# GEMM K-loops: the redundant s_waitcnt lgkmcnt(0) directly after the pre-MFMA barrier removed (24 sites); the same wait already precedes the barrier and nothing is issued in between
# speedup vs baseline: 1.0048x; 1.0043x over previous
; #define PG8_STAGE_A(bufoff, base_, nx_, kb_, h_) do { if (GATHER) { if (nx_) PG8_STAGE_G(bufoff, kb_, goN, h_); else PG8_STAGE_G(bufoff, kb_, goC, h_); } \
;         else PG8_STAGE(bufoff, (base_) + (kb_) + (h_) * hstep, voffA); } while (0)
; #define PG8_STAGE(bufoff, gbase, voff) do { _Pragma("unroll") for (int _i = 0; _i < 2; ++_i) \
;         __builtin_amdgcn_global_load_lds((const unsigned*)((const char*)(gbase) + (voff)[_i]), (LAS unsigned*)(lds + (bufoff) + ldsw + _i * 8192), 16, 0, 0); } while (0)
; #define PG8_LDA(dst, b, h) do { _Pragma("unroll") for (int m = 0; m < 4; ++m) _Pragma("unroll") for (int k = 0; k < 2; ++k) dst[m][k] = *(const LAS bf16x8*)(lds + PG8_SA(b, h) + aoff + m * 2048 + k * 1024); } while (0)
; #define PG8_LDB(dst, b, h) do { _Pragma("unroll") for (int n = 0; n < 2; ++n) _Pragma("unroll") for (int k = 0; k < 2; ++k) dst[n][k] = *(const LAS bf16x8*)(lds + PG8_SB(b, h) + boff + n * 2048 + k * 1024); } while (0)
; #define PG8_MMA(ai, bj, At, Bt) do { __builtin_amdgcn_s_setprio(1); _Pragma("unroll") for (int m = 0; m < 4; ++m) _Pragma("unroll") for (int n = 0; n < 2; ++n) _Pragma("unroll") for (int k = 0; k < 2; ++k) \
;         acc[ai][bj][m][n] = __builtin_amdgcn_mfma_f32_16x16x32_bf16(Bt[n][k], At[m][k], acc[ai][bj][m][n], 0, 0, 0); __builtin_amdgcn_s_setprio(0); } while (0)
; #define PG8_WAIT_V(n) asm volatile("s_waitcnt vmcnt(" #n ")" ::: "memory")
; #define PG8_WAIT_L(n) asm volatile("s_waitcnt lgkmcnt(" #n ")" ::: "memory")
; #define PG8_BAR __builtin_amdgcn_s_barrier()
; #define PG8_SCHED __builtin_amdgcn_sched_barrier(0)
; template <class Epi, class Sched, bool GATHER = false>
; __device__ __forceinline__ void gemm_phase(LAS unsigned char* lds, const Gemm g, const Sched& S, const Epi& E, const int tid) {
;     ...
;             PG8_LDB(B0, 0, 0); PG8_LDB(B1, 0, 1); PG8_SCHED; PG8_LDA(At, 0, 0); PG8_STAGE_A(PG8_SA(1, 1), cA, false, kb1, 1);
;             PG8_WAIT_V(8); PG8_WAIT_L(0); PG8_BAR; PG8_MMA(0, 0, At, B0); PG8_MMA(0, 1, At, B1); PG8_BAR; PG8_SCHED;
;             PG8_LDA(At, 0, 1); PG8_STAGE(PG8_SB(0, 0), b2, voffB); PG8_STAGE(PG8_SB(0, 1), b2 + hstep, voffB); PG8_STAGE_A(PG8_SA(0, 0), (last ? nA : cA), last, kb2, 0);
;             PG8_WAIT_V(8); PG8_WAIT_L(0); PG8_BAR; PG8_MMA(1, 0, At, B0); PG8_MMA(1, 1, At, B1); PG8_BAR; PG8_SCHED;
.LBB0_247:
	s_add_u32 s22, s28, 0x100
	s_addc_u32 s23, s29, 0
	s_add_u32 s54, s49, s28
	s_addc_u32 s55, s50, s29
	s_add_i32 s24, 0, 0x10000
	s_add_i32 s56, 0, 0x14000
	v_add_u32_e32 v2, s24, v1
	ds_read_b128 v[152:155], v2
	ds_read_b128 v[156:159], v2 offset:1024
	ds_read_b128 v[160:163], v2 offset:2048
	ds_read_b128 v[164:167], v2 offset:3072
	v_add_u32_e32 v2, s56, v1
	ds_read_b128 v[168:171], v2
	ds_read_b128 v[172:175], v2 offset:1024
	ds_read_b128 v[176:179], v2 offset:2048
	ds_read_b128 v[180:183], v2 offset:3072
	s_add_i32 s58, s24, s38
	s_add_i32 m0, s11, 0xc000
	s_add_i32 s57, s11, 0xe000
	s_add_i32 s59, s58, 0x2000
	s_cmp_eq_u32 s51, 28
	s_cselect_b64 s[52:53], -1, 0
	s_and_b64 s[24:25], s[52:53], exec
	s_cselect_b32 s25, s13, s55
	s_cselect_b32 s24, s15, s54
	v_lshl_add_u64 v[218:219], v[4:5], 0, s[28:29]
	ds_read_b128 v[184:187], v150
	ds_read_b128 v[188:191], v150 offset:1024
	ds_read_b128 v[192:195], v150 offset:2048
	ds_read_b128 v[196:199], v150 offset:3072
	ds_read_b128 v[202:205], v150 offset:4096
	ds_read_b128 v[206:209], v150 offset:5120
	ds_read_b128 v[210:213], v150 offset:6144
	ds_read_b128 v[214:217], v150 offset:7168
	global_load_lds_dwordx4 v[218:219], off
	v_lshl_add_u64 v[218:219], v[146:147], 0, s[28:29]
	s_mov_b32 m0, s57
	s_nop 0
	global_load_lds_dwordx4 v[218:219], off
	s_waitcnt vmcnt(8)
	s_waitcnt lgkmcnt(0)
	s_barrier
	v_mfma_f32_16x16x32_bf16 v[14:17], v[152:155], v[184:187], v[14:17]
	v_mfma_f32_16x16x32_bf16 v[10:13], v[160:163], v[184:187], v[10:13]
	v_mfma_f32_16x16x32_bf16 v[6:9], v[152:155], v[192:195], v[6:9]
	v_mfma_f32_16x16x32_bf16 v[18:21], v[160:163], v[192:195], v[18:21]
	v_mfma_f32_16x16x32_bf16 v[22:25], v[152:155], v[202:205], v[22:25]
	v_mfma_f32_16x16x32_bf16 v[34:37], v[160:163], v[202:205], v[34:37]
	v_mfma_f32_16x16x32_bf16 v[26:29], v[152:155], v[210:213], v[26:29]
	v_mfma_f32_16x16x32_bf16 v[30:33], v[160:163], v[210:213], v[30:33]
	v_mfma_f32_16x16x32_bf16 v[14:17], v[156:159], v[188:191], v[14:17]
	v_mfma_f32_16x16x32_bf16 v[10:13], v[164:167], v[188:191], v[10:13]
	v_mfma_f32_16x16x32_bf16 v[6:9], v[156:159], v[196:199], v[6:9]
	v_mfma_f32_16x16x32_bf16 v[18:21], v[164:167], v[196:199], v[18:21]
	v_mfma_f32_16x16x32_bf16 v[22:25], v[156:159], v[206:209], v[22:25]
	v_mfma_f32_16x16x32_bf16 v[34:37], v[164:167], v[206:209], v[34:37]
	v_mfma_f32_16x16x32_bf16 v[26:29], v[156:159], v[214:217], v[26:29]
	v_mfma_f32_16x16x32_bf16 v[30:33], v[164:167], v[214:217], v[30:33]
	v_mfma_f32_16x16x32_bf16 v[66:69], v[168:171], v[184:187], v[66:69]
	v_mfma_f32_16x16x32_bf16 v[98:101], v[176:179], v[184:187], v[98:101]
	v_mfma_f32_16x16x32_bf16 v[62:65], v[168:171], v[192:195], v[62:65]
	v_mfma_f32_16x16x32_bf16 v[94:97], v[176:179], v[192:195], v[94:97]
	v_mfma_f32_16x16x32_bf16 v[58:61], v[168:171], v[202:205], v[58:61]
	v_mfma_f32_16x16x32_bf16 v[90:93], v[176:179], v[202:205], v[90:93]
	v_mfma_f32_16x16x32_bf16 v[54:57], v[168:171], v[210:213], v[54:57]
	v_mfma_f32_16x16x32_bf16 v[86:89], v[176:179], v[210:213], v[86:89]
	v_mfma_f32_16x16x32_bf16 v[66:69], v[172:175], v[188:191], v[66:69]
	v_mfma_f32_16x16x32_bf16 v[98:101], v[180:183], v[188:191], v[98:101]
	v_mfma_f32_16x16x32_bf16 v[62:65], v[172:175], v[196:199], v[62:65]
	v_mfma_f32_16x16x32_bf16 v[94:97], v[180:183], v[196:199], v[94:97]
	v_mfma_f32_16x16x32_bf16 v[58:61], v[172:175], v[206:209], v[58:61]
	v_mfma_f32_16x16x32_bf16 v[90:93], v[180:183], v[206:209], v[90:93]
	v_mfma_f32_16x16x32_bf16 v[54:57], v[172:175], v[214:217], v[54:57]
	v_mfma_f32_16x16x32_bf16 v[86:89], v[180:183], v[214:217], v[86:89]
	s_barrier
	s_mov_b32 m0, s58
	v_lshl_add_u64 v[218:219], s[24:25], 0, v[138:139]
	s_cselect_b32 s54, 0, s23
	s_cselect_b32 s55, 0, s22
	s_add_u32 s28, s24, 0x80000
	ds_read_b128 v[184:187], v150 offset:16384
	ds_read_b128 v[188:191], v150 offset:17408
	ds_read_b128 v[192:195], v150 offset:18432
	ds_read_b128 v[196:199], v150 offset:19456
	ds_read_b128 v[202:205], v150 offset:20480
	ds_read_b128 v[206:209], v150 offset:21504
	ds_read_b128 v[210:213], v150 offset:22528
	ds_read_b128 v[214:217], v150 offset:23552
	global_load_lds_dwordx4 v[218:219], off
	v_lshl_add_u64 v[220:221], s[24:25], 0, v[134:135]
	s_mov_b32 m0, s59
	s_addc_u32 s29, s25, 0
	s_add_i32 s56, s56, s38
	global_load_lds_dwordx4 v[220:221], off
	v_lshl_add_u64 v[222:223], s[28:29], 0, v[138:139]
	s_mov_b32 m0, s56
	s_nop 0
	global_load_lds_dwordx4 v[222:223], off
	v_lshl_add_u64 v[222:223], s[28:29], 0, v[134:135]
	s_add_i32 m0, s56, 0x2000
	s_and_b64 s[28:29], s[52:53], s[4:5]
	s_and_b64 s[28:29], s[28:29], exec
	s_cselect_b32 s28, s18, s16
	s_cselect_b32 s29, s19, s17
	s_add_u32 s28, s28, s55
	s_addc_u32 s29, s29, s54
	global_load_lds_dwordx4 v[222:223], off
	v_lshl_add_u64 v[222:223], s[28:29], 0, v[140:141]
	s_mov_b32 m0, s11
	v_lshl_add_u64 v[224:225], s[28:29], 0, v[136:137]
	global_load_lds_dwordx4 v[222:223], off
	s_mov_b32 m0, s40
	s_nop 0
	global_load_lds_dwordx4 v[224:225], off
	s_waitcnt vmcnt(8)
	s_waitcnt lgkmcnt(0)
	s_barrier
; #define PG8_STAGE_A(bufoff, base_, nx_, kb_, h_) do { if (GATHER) { if (nx_) PG8_STAGE_G(bufoff, kb_, goN, h_); else PG8_STAGE_G(bufoff, kb_, goC, h_); } \
;         else PG8_STAGE(bufoff, (base_) + (kb_) + (h_) * hstep, voffA); } while (0)
; #define PG8_LDA(dst, b, h) do { _Pragma("unroll") for (int m = 0; m < 4; ++m) _Pragma("unroll") for (int k = 0; k < 2; ++k) dst[m][k] = *(const LAS bf16x8*)(lds + PG8_SA(b, h) + aoff + m * 2048 + k * 1024); } while (0)
; #define PG8_LDB(dst, b, h) do { _Pragma("unroll") for (int n = 0; n < 2; ++n) _Pragma("unroll") for (int k = 0; k < 2; ++k) dst[n][k] = *(const LAS bf16x8*)(lds + PG8_SB(b, h) + boff + n * 2048 + k * 1024); } while (0)
; #define PG8_MMA(ai, bj, At, Bt) do { __builtin_amdgcn_s_setprio(1); _Pragma("unroll") for (int m = 0; m < 4; ++m) _Pragma("unroll") for (int n = 0; n < 2; ++n) _Pragma("unroll") for (int k = 0; k < 2; ++k) \
;         acc[ai][bj][m][n] = __builtin_amdgcn_mfma_f32_16x16x32_bf16(Bt[n][k], At[m][k], acc[ai][bj][m][n], 0, 0, 0); __builtin_amdgcn_s_setprio(0); } while (0)
; #define PG8_WAIT_V(n) asm volatile("s_waitcnt vmcnt(" #n ")" ::: "memory")
; #define PG8_WAIT_L(n) asm volatile("s_waitcnt lgkmcnt(" #n ")" ::: "memory")
; #define PG8_BAR __builtin_amdgcn_s_barrier()
; #define PG8_SCHED __builtin_amdgcn_sched_barrier(0)
; template <class Epi, class Sched, bool GATHER = false>
; __device__ __forceinline__ void gemm_phase(LAS unsigned char* lds, const Gemm g, const Sched& S, const Epi& E, const int tid) {
;     ...
;             PG8_WAIT_V(8); PG8_WAIT_L(0); PG8_BAR; PG8_MMA(1, 0, At, B0); PG8_MMA(1, 1, At, B1); PG8_BAR; PG8_SCHED;
;             PG8_LDB(B0, 1, 0); PG8_LDB(B1, 1, 1); PG8_SCHED; PG8_LDA(At, 1, 0); PG8_STAGE_A(PG8_SA(0, 1), (last ? nA : cA), last, kb2, 1);
;             PG8_WAIT_V(8); PG8_WAIT_L(0); PG8_BAR; PG8_MMA(0, 0, At, B0); PG8_MMA(0, 1, At, B1); PG8_BAR; PG8_SCHED;
	v_mfma_f32_16x16x32_bf16 v[50:53], v[152:155], v[184:187], v[50:53]
	v_mfma_f32_16x16x32_bf16 v[82:85], v[160:163], v[184:187], v[82:85]
	v_mfma_f32_16x16x32_bf16 v[46:49], v[152:155], v[192:195], v[46:49]
	v_mfma_f32_16x16x32_bf16 v[78:81], v[160:163], v[192:195], v[78:81]
	v_mfma_f32_16x16x32_bf16 v[42:45], v[152:155], v[202:205], v[42:45]
	v_mfma_f32_16x16x32_bf16 v[74:77], v[160:163], v[202:205], v[74:77]
	v_mfma_f32_16x16x32_bf16 v[38:41], v[152:155], v[210:213], v[38:41]
	v_mfma_f32_16x16x32_bf16 v[70:73], v[160:163], v[210:213], v[70:73]
	v_mfma_f32_16x16x32_bf16 v[50:53], v[156:159], v[188:191], v[50:53]
	v_mfma_f32_16x16x32_bf16 v[82:85], v[164:167], v[188:191], v[82:85]
	v_mfma_f32_16x16x32_bf16 v[46:49], v[156:159], v[196:199], v[46:49]
	v_mfma_f32_16x16x32_bf16 v[78:81], v[164:167], v[196:199], v[78:81]
	v_mfma_f32_16x16x32_bf16 v[42:45], v[156:159], v[206:209], v[42:45]
	v_mfma_f32_16x16x32_bf16 v[74:77], v[164:167], v[206:209], v[74:77]
	v_mfma_f32_16x16x32_bf16 v[38:41], v[156:159], v[214:217], v[38:41]
	v_mfma_f32_16x16x32_bf16 v[70:73], v[164:167], v[214:217], v[70:73]
	v_mfma_f32_16x16x32_bf16 v[114:117], v[168:171], v[184:187], v[114:117]
	v_mfma_f32_16x16x32_bf16 v[130:133], v[176:179], v[184:187], v[130:133]
	v_mfma_f32_16x16x32_bf16 v[110:113], v[168:171], v[192:195], v[110:113]
	v_mfma_f32_16x16x32_bf16 v[126:129], v[176:179], v[192:195], v[126:129]
	v_mfma_f32_16x16x32_bf16 v[106:109], v[168:171], v[202:205], v[106:109]
	v_mfma_f32_16x16x32_bf16 v[122:125], v[176:179], v[202:205], v[122:125]
	v_mfma_f32_16x16x32_bf16 v[102:105], v[168:171], v[210:213], v[102:105]
	v_mfma_f32_16x16x32_bf16 v[118:121], v[176:179], v[210:213], v[118:121]
	v_mfma_f32_16x16x32_bf16 v[114:117], v[172:175], v[188:191], v[114:117]
	v_mfma_f32_16x16x32_bf16 v[130:133], v[180:183], v[188:191], v[130:133]
	v_mfma_f32_16x16x32_bf16 v[110:113], v[172:175], v[196:199], v[110:113]
	v_mfma_f32_16x16x32_bf16 v[126:129], v[180:183], v[196:199], v[126:129]
	v_mfma_f32_16x16x32_bf16 v[106:109], v[172:175], v[206:209], v[106:109]
	v_mfma_f32_16x16x32_bf16 v[122:125], v[180:183], v[206:209], v[122:125]
	v_mfma_f32_16x16x32_bf16 v[102:105], v[172:175], v[214:217], v[102:105]
	v_mfma_f32_16x16x32_bf16 v[118:121], v[180:183], v[214:217], v[118:121]
	s_barrier
	s_add_i32 s52, 0, 0x18000
	v_add_u32_e32 v2, s52, v1
	s_add_i32 s53, 0, 0x1c000
	ds_read_b128 v[152:155], v2
	ds_read_b128 v[156:159], v2 offset:1024
	ds_read_b128 v[160:163], v2 offset:2048
	ds_read_b128 v[164:167], v2 offset:3072
	v_add_u32_e32 v2, s53, v1
	ds_read_b128 v[168:171], v2
	ds_read_b128 v[172:175], v2 offset:1024
	ds_read_b128 v[176:179], v2 offset:2048
	ds_read_b128 v[180:183], v2 offset:3072
	s_add_u32 s28, s28, 0x80000
	s_addc_u32 s29, s29, 0
	s_mov_b32 m0, s41
	v_lshl_add_u64 v[226:227], s[28:29], 0, v[140:141]
	ds_read_b128 v[184:187], v150 offset:32768
	ds_read_b128 v[188:191], v150 offset:33792
	ds_read_b128 v[192:195], v150 offset:34816
	ds_read_b128 v[196:199], v150 offset:35840
	ds_read_b128 v[202:205], v150 offset:36864
	ds_read_b128 v[206:209], v150 offset:37888
	ds_read_b128 v[210:213], v150 offset:38912
	ds_read_b128 v[214:217], v150 offset:39936
	global_load_lds_dwordx4 v[226:227], off
	v_lshl_add_u64 v[226:227], s[28:29], 0, v[136:137]
	s_mov_b32 m0, s42
	s_nop 0
	global_load_lds_dwordx4 v[226:227], off
	s_waitcnt vmcnt(8)
	s_waitcnt lgkmcnt(0)
	s_barrier
	v_mfma_f32_16x16x32_bf16 v[14:17], v[152:155], v[184:187], v[14:17]
	v_mfma_f32_16x16x32_bf16 v[10:13], v[160:163], v[184:187], v[10:13]
	v_mfma_f32_16x16x32_bf16 v[6:9], v[152:155], v[192:195], v[6:9]
	v_mfma_f32_16x16x32_bf16 v[18:21], v[160:163], v[192:195], v[18:21]
	v_mfma_f32_16x16x32_bf16 v[22:25], v[152:155], v[202:205], v[22:25]
	v_mfma_f32_16x16x32_bf16 v[34:37], v[160:163], v[202:205], v[34:37]
	v_mfma_f32_16x16x32_bf16 v[26:29], v[152:155], v[210:213], v[26:29]
	v_mfma_f32_16x16x32_bf16 v[30:33], v[160:163], v[210:213], v[30:33]
	v_mfma_f32_16x16x32_bf16 v[14:17], v[156:159], v[188:191], v[14:17]
	v_mfma_f32_16x16x32_bf16 v[10:13], v[164:167], v[188:191], v[10:13]
	v_mfma_f32_16x16x32_bf16 v[6:9], v[156:159], v[196:199], v[6:9]
	v_mfma_f32_16x16x32_bf16 v[18:21], v[164:167], v[196:199], v[18:21]
	v_mfma_f32_16x16x32_bf16 v[22:25], v[156:159], v[206:209], v[22:25]
	v_mfma_f32_16x16x32_bf16 v[34:37], v[164:167], v[206:209], v[34:37]
	v_mfma_f32_16x16x32_bf16 v[26:29], v[156:159], v[214:217], v[26:29]
	v_mfma_f32_16x16x32_bf16 v[30:33], v[164:167], v[214:217], v[30:33]
	v_mfma_f32_16x16x32_bf16 v[66:69], v[168:171], v[184:187], v[66:69]
	v_mfma_f32_16x16x32_bf16 v[98:101], v[176:179], v[184:187], v[98:101]
	v_mfma_f32_16x16x32_bf16 v[62:65], v[168:171], v[192:195], v[62:65]
	v_mfma_f32_16x16x32_bf16 v[94:97], v[176:179], v[192:195], v[94:97]
	v_mfma_f32_16x16x32_bf16 v[58:61], v[168:171], v[202:205], v[58:61]
	v_mfma_f32_16x16x32_bf16 v[90:93], v[176:179], v[202:205], v[90:93]
	v_mfma_f32_16x16x32_bf16 v[54:57], v[168:171], v[210:213], v[54:57]
	v_mfma_f32_16x16x32_bf16 v[86:89], v[176:179], v[210:213], v[86:89]
	v_mfma_f32_16x16x32_bf16 v[66:69], v[172:175], v[188:191], v[66:69]
	v_mfma_f32_16x16x32_bf16 v[98:101], v[180:183], v[188:191], v[98:101]
	v_mfma_f32_16x16x32_bf16 v[62:65], v[172:175], v[196:199], v[62:65]
	v_mfma_f32_16x16x32_bf16 v[94:97], v[180:183], v[196:199], v[94:97]
	v_mfma_f32_16x16x32_bf16 v[58:61], v[172:175], v[206:209], v[58:61]
	v_mfma_f32_16x16x32_bf16 v[90:93], v[180:183], v[206:209], v[90:93]
	v_mfma_f32_16x16x32_bf16 v[54:57], v[172:175], v[214:217], v[54:57]
	v_mfma_f32_16x16x32_bf16 v[86:89], v[180:183], v[214:217], v[86:89]
	s_barrier
; #define PG8_STAGE_A(bufoff, base_, nx_, kb_, h_) do { if (GATHER) { if (nx_) PG8_STAGE_G(bufoff, kb_, goN, h_); else PG8_STAGE_G(bufoff, kb_, goC, h_); } \
;         else PG8_STAGE(bufoff, (base_) + (kb_) + (h_) * hstep, voffA); } while (0)
; #define PG8_STAGE(bufoff, gbase, voff) do { _Pragma("unroll") for (int _i = 0; _i < 2; ++_i) \
;         __builtin_amdgcn_global_load_lds((const unsigned*)((const char*)(gbase) + (voff)[_i]), (LAS unsigned*)(lds + (bufoff) + ldsw + _i * 8192), 16, 0, 0); } while (0)
; #define PG8_LDA(dst, b, h) do { _Pragma("unroll") for (int m = 0; m < 4; ++m) _Pragma("unroll") for (int k = 0; k < 2; ++k) dst[m][k] = *(const LAS bf16x8*)(lds + PG8_SA(b, h) + aoff + m * 2048 + k * 1024); } while (0)
; #define PG8_MMA(ai, bj, At, Bt) do { __builtin_amdgcn_s_setprio(1); _Pragma("unroll") for (int m = 0; m < 4; ++m) _Pragma("unroll") for (int n = 0; n < 2; ++n) _Pragma("unroll") for (int k = 0; k < 2; ++k) \
;         acc[ai][bj][m][n] = __builtin_amdgcn_mfma_f32_16x16x32_bf16(Bt[n][k], At[m][k], acc[ai][bj][m][n], 0, 0, 0); __builtin_amdgcn_s_setprio(0); } while (0)
; #define PG8_WAIT_V(n) asm volatile("s_waitcnt vmcnt(" #n ")" ::: "memory")
; #define PG8_WAIT_L(n) asm volatile("s_waitcnt lgkmcnt(" #n ")" ::: "memory")
; #define PG8_BAR __builtin_amdgcn_s_barrier()
; #define PG8_SCHED __builtin_amdgcn_sched_barrier(0)
; template <class Epi, class Sched, bool GATHER = false>
; __device__ __forceinline__ void gemm_phase(LAS unsigned char* lds, const Gemm g, const Sched& S, const Epi& E, const int tid) {
;     ...
;             PG8_LDA(At, 1, 1); PG8_STAGE(PG8_SB(1, 0), b3, voffB); PG8_STAGE(PG8_SB(1, 1), b3 + hstep, voffB); PG8_STAGE_A(PG8_SA(1, 0), (last ? nA : cA), last, kb3, 0);
;             PG8_WAIT_V(8); PG8_WAIT_L(0); PG8_BAR; PG8_MMA(1, 0, At, B0); PG8_MMA(1, 1, At, B1); PG8_BAR; PG8_SCHED;
;     ...
;         }
;         if (wr == 0) PG8_BAR;
	s_add_i32 s28, s52, s38
	v_lshl_add_u64 v[218:219], v[218:219], 0, s[0:1]
	s_mov_b32 m0, s28
	ds_read_b128 v[184:187], v150 offset:49152
	ds_read_b128 v[188:191], v150 offset:50176
	ds_read_b128 v[192:195], v150 offset:51200
	ds_read_b128 v[196:199], v150 offset:52224
	ds_read_b128 v[202:205], v150 offset:53248
	ds_read_b128 v[206:209], v150 offset:54272
	ds_read_b128 v[210:213], v150 offset:55296
	ds_read_b128 v[214:217], v150 offset:56320
	global_load_lds_dwordx4 v[218:219], off
	s_add_i32 m0, s28, 0x2000
	s_add_u32 s24, s24, 0x80080
	v_lshl_add_u64 v[218:219], v[220:221], 0, s[0:1]
	s_addc_u32 s25, s25, 0
	s_add_i32 s28, s53, s38
	global_load_lds_dwordx4 v[218:219], off
	v_lshl_add_u64 v[218:219], s[24:25], 0, v[138:139]
	s_mov_b32 m0, s28
	s_nop 0
	global_load_lds_dwordx4 v[218:219], off
	v_lshl_add_u64 v[218:219], s[24:25], 0, v[134:135]
	s_add_i32 m0, s28, 0x2000
	s_nop 0
	global_load_lds_dwordx4 v[218:219], off
	v_lshl_add_u64 v[218:219], v[222:223], 0, s[0:1]
	s_mov_b32 m0, s44
	s_nop 0
	global_load_lds_dwordx4 v[218:219], off
	v_lshl_add_u64 v[218:219], v[224:225], 0, s[0:1]
	s_mov_b32 m0, s45
	s_nop 0
	global_load_lds_dwordx4 v[218:219], off
	s_waitcnt vmcnt(8)
	s_waitcnt lgkmcnt(0)
	s_barrier
	v_mfma_f32_16x16x32_bf16 v[50:53], v[152:155], v[184:187], v[50:53]
	v_mfma_f32_16x16x32_bf16 v[82:85], v[160:163], v[184:187], v[82:85]
	v_mfma_f32_16x16x32_bf16 v[46:49], v[152:155], v[192:195], v[46:49]
	v_mfma_f32_16x16x32_bf16 v[78:81], v[160:163], v[192:195], v[78:81]
	v_mfma_f32_16x16x32_bf16 v[42:45], v[152:155], v[202:205], v[42:45]
	v_mfma_f32_16x16x32_bf16 v[74:77], v[160:163], v[202:205], v[74:77]
	v_mfma_f32_16x16x32_bf16 v[38:41], v[152:155], v[210:213], v[38:41]
	v_mfma_f32_16x16x32_bf16 v[70:73], v[160:163], v[210:213], v[70:73]
	v_mfma_f32_16x16x32_bf16 v[50:53], v[156:159], v[188:191], v[50:53]
	v_mfma_f32_16x16x32_bf16 v[82:85], v[164:167], v[188:191], v[82:85]
	v_mfma_f32_16x16x32_bf16 v[46:49], v[156:159], v[196:199], v[46:49]
	v_mfma_f32_16x16x32_bf16 v[78:81], v[164:167], v[196:199], v[78:81]
	v_mfma_f32_16x16x32_bf16 v[42:45], v[156:159], v[206:209], v[42:45]
	v_mfma_f32_16x16x32_bf16 v[74:77], v[164:167], v[206:209], v[74:77]
	v_mfma_f32_16x16x32_bf16 v[38:41], v[156:159], v[214:217], v[38:41]
	v_mfma_f32_16x16x32_bf16 v[70:73], v[164:167], v[214:217], v[70:73]
	v_mfma_f32_16x16x32_bf16 v[114:117], v[168:171], v[184:187], v[114:117]
	v_mfma_f32_16x16x32_bf16 v[130:133], v[176:179], v[184:187], v[130:133]
	v_mfma_f32_16x16x32_bf16 v[110:113], v[168:171], v[192:195], v[110:113]
	v_mfma_f32_16x16x32_bf16 v[126:129], v[176:179], v[192:195], v[126:129]
	v_mfma_f32_16x16x32_bf16 v[106:109], v[168:171], v[202:205], v[106:109]
	v_mfma_f32_16x16x32_bf16 v[122:125], v[176:179], v[202:205], v[122:125]
	v_mfma_f32_16x16x32_bf16 v[102:105], v[168:171], v[210:213], v[102:105]
	v_mfma_f32_16x16x32_bf16 v[118:121], v[176:179], v[210:213], v[118:121]
	v_mfma_f32_16x16x32_bf16 v[114:117], v[172:175], v[188:191], v[114:117]
	v_mfma_f32_16x16x32_bf16 v[130:133], v[180:183], v[188:191], v[130:133]
	v_mfma_f32_16x16x32_bf16 v[110:113], v[172:175], v[196:199], v[110:113]
	v_mfma_f32_16x16x32_bf16 v[126:129], v[180:183], v[196:199], v[126:129]
	v_mfma_f32_16x16x32_bf16 v[106:109], v[172:175], v[206:209], v[106:109]
	v_mfma_f32_16x16x32_bf16 v[122:125], v[180:183], v[206:209], v[122:125]
	v_mfma_f32_16x16x32_bf16 v[102:105], v[172:175], v[214:217], v[102:105]
	v_mfma_f32_16x16x32_bf16 v[118:121], v[180:183], v[214:217], v[118:121]
	s_barrier
	s_add_i32 s51, s51, 2
	s_cmp_gt_u32 s51, 29
	s_mov_b64 s[28:29], s[22:23]
	s_cbranch_scc0 .LBB0_247
	s_and_b64 vcc, exec, s[8:9]
	s_cbranch_vccz .LBB0_250
	s_barrier

; #define PG8_STAGE_A(bufoff, base_, nx_, kb_, h_) do { if (GATHER) { if (nx_) PG8_STAGE_G(bufoff, kb_, goN, h_); else PG8_STAGE_G(bufoff, kb_, goC, h_); } \
;         else PG8_STAGE(bufoff, (base_) + (kb_) + (h_) * hstep, voffA); } while (0)
; #define PG8_STAGE(bufoff, gbase, voff) do { _Pragma("unroll") for (int _i = 0; _i < 2; ++_i) \
;         __builtin_amdgcn_global_load_lds((const unsigned*)((const char*)(gbase) + (voff)[_i]), (LAS unsigned*)(lds + (bufoff) + ldsw + _i * 8192), 16, 0, 0); } while (0)
; #define PG8_LDA(dst, b, h) do { _Pragma("unroll") for (int m = 0; m < 4; ++m) _Pragma("unroll") for (int k = 0; k < 2; ++k) dst[m][k] = *(const LAS bf16x8*)(lds + PG8_SA(b, h) + aoff + m * 2048 + k * 1024); } while (0)
; #define PG8_LDB(dst, b, h) do { _Pragma("unroll") for (int n = 0; n < 2; ++n) _Pragma("unroll") for (int k = 0; k < 2; ++k) dst[n][k] = *(const LAS bf16x8*)(lds + PG8_SB(b, h) + boff + n * 2048 + k * 1024); } while (0)
; #define PG8_MMA(ai, bj, At, Bt) do { __builtin_amdgcn_s_setprio(1); _Pragma("unroll") for (int m = 0; m < 4; ++m) _Pragma("unroll") for (int n = 0; n < 2; ++n) _Pragma("unroll") for (int k = 0; k < 2; ++k) \
;         acc[ai][bj][m][n] = __builtin_amdgcn_mfma_f32_16x16x32_bf16(Bt[n][k], At[m][k], acc[ai][bj][m][n], 0, 0, 0); __builtin_amdgcn_s_setprio(0); } while (0)
; #define PG8_WAIT_V(n) asm volatile("s_waitcnt vmcnt(" #n ")" ::: "memory")
; #define PG8_WAIT_L(n) asm volatile("s_waitcnt lgkmcnt(" #n ")" ::: "memory")
; #define PG8_BAR __builtin_amdgcn_s_barrier()
; #define PG8_SCHED __builtin_amdgcn_sched_barrier(0)
; template <class Epi, class Sched, bool GATHER = false>
; __device__ __forceinline__ void gemm_phase(LAS unsigned char* lds, const Gemm g, const Sched& S, const Epi& E, const int tid) {
;     ...
;             PG8_LDB(B0, 0, 0); PG8_LDB(B1, 0, 1); PG8_SCHED; PG8_LDA(At, 0, 0); PG8_STAGE_A(PG8_SA(1, 1), cA, false, kb1, 1);
;             PG8_WAIT_V(8); PG8_WAIT_L(0); PG8_BAR; PG8_MMA(0, 0, At, B0); PG8_MMA(0, 1, At, B1); PG8_BAR; PG8_SCHED;
;             PG8_LDA(At, 0, 1); PG8_STAGE(PG8_SB(0, 0), b2, voffB); PG8_STAGE(PG8_SB(0, 1), b2 + hstep, voffB); PG8_STAGE_A(PG8_SA(0, 0), (last ? nA : cA), last, kb2, 0);
;             PG8_WAIT_V(8); PG8_WAIT_L(0); PG8_BAR; PG8_MMA(1, 0, At, B0); PG8_MMA(1, 1, At, B1); PG8_BAR; PG8_SCHED;
.LBB0_1128:
	s_add_u32 s22, s28, 0x100
	s_addc_u32 s23, s29, 0
	s_add_u32 s52, s47, s28
	s_addc_u32 s53, s48, s29
	s_add_i32 s24, 0, 0x10000
	s_add_i32 s54, 0, 0x14000
	v_add_u32_e32 v2, s24, v148
	ds_read_b128 v[152:155], v2
	ds_read_b128 v[156:159], v2 offset:1024
	ds_read_b128 v[160:163], v2 offset:2048
	ds_read_b128 v[164:167], v2 offset:3072
	v_add_u32_e32 v2, s54, v148
	ds_read_b128 v[168:171], v2
	ds_read_b128 v[172:175], v2 offset:1024
	ds_read_b128 v[176:179], v2 offset:2048
	ds_read_b128 v[180:183], v2 offset:3072
	s_add_i32 s56, s24, s33
	s_add_i32 m0, s9, 0xc000
	s_add_i32 s55, s9, 0xe000
	s_add_i32 s57, s56, 0x2000
	s_cmp_eq_u32 s49, 28
	s_cselect_b64 s[50:51], -1, 0
	s_and_b64 s[24:25], s[50:51], exec
	s_cselect_b32 s25, s15, s53
	s_cselect_b32 s24, s17, s52
	v_lshl_add_u64 v[218:219], v[4:5], 0, s[28:29]
	ds_read_b128 v[184:187], v150
	ds_read_b128 v[188:191], v150 offset:1024
	ds_read_b128 v[192:195], v150 offset:2048
	ds_read_b128 v[196:199], v150 offset:3072
	ds_read_b128 v[202:205], v150 offset:4096
	ds_read_b128 v[206:209], v150 offset:5120
	ds_read_b128 v[210:213], v150 offset:6144
	ds_read_b128 v[214:217], v150 offset:7168
	global_load_lds_dwordx4 v[218:219], off
	v_lshl_add_u64 v[218:219], v[146:147], 0, s[28:29]
	s_mov_b32 m0, s55
	s_nop 0
	global_load_lds_dwordx4 v[218:219], off
	s_waitcnt vmcnt(8)
	s_waitcnt lgkmcnt(0)
	s_barrier
	v_mfma_f32_16x16x32_bf16 v[86:89], v[152:155], v[184:187], v[86:89]
	v_mfma_f32_16x16x32_bf16 v[18:21], v[160:163], v[184:187], v[18:21]
	v_mfma_f32_16x16x32_bf16 v[6:9], v[152:155], v[192:195], v[6:9]
	v_mfma_f32_16x16x32_bf16 v[22:25], v[160:163], v[192:195], v[22:25]
	v_mfma_f32_16x16x32_bf16 v[10:13], v[152:155], v[202:205], v[10:13]
	v_mfma_f32_16x16x32_bf16 v[26:29], v[160:163], v[202:205], v[26:29]
	v_mfma_f32_16x16x32_bf16 v[14:17], v[152:155], v[210:213], v[14:17]
	v_mfma_f32_16x16x32_bf16 v[30:33], v[160:163], v[210:213], v[30:33]
	v_mfma_f32_16x16x32_bf16 v[86:89], v[156:159], v[188:191], v[86:89]
	v_mfma_f32_16x16x32_bf16 v[18:21], v[164:167], v[188:191], v[18:21]
	v_mfma_f32_16x16x32_bf16 v[6:9], v[156:159], v[196:199], v[6:9]
	v_mfma_f32_16x16x32_bf16 v[22:25], v[164:167], v[196:199], v[22:25]
	v_mfma_f32_16x16x32_bf16 v[10:13], v[156:159], v[206:209], v[10:13]
	v_mfma_f32_16x16x32_bf16 v[26:29], v[164:167], v[206:209], v[26:29]
	v_mfma_f32_16x16x32_bf16 v[14:17], v[156:159], v[214:217], v[14:17]
	v_mfma_f32_16x16x32_bf16 v[30:33], v[164:167], v[214:217], v[30:33]
	v_mfma_f32_16x16x32_bf16 v[34:37], v[168:171], v[184:187], v[34:37]
	v_mfma_f32_16x16x32_bf16 v[50:53], v[176:179], v[184:187], v[50:53]
	v_mfma_f32_16x16x32_bf16 v[38:41], v[168:171], v[192:195], v[38:41]
	v_mfma_f32_16x16x32_bf16 v[58:61], v[176:179], v[192:195], v[58:61]
	v_mfma_f32_16x16x32_bf16 v[42:45], v[168:171], v[202:205], v[42:45]
	v_mfma_f32_16x16x32_bf16 v[66:69], v[176:179], v[202:205], v[66:69]
	v_mfma_f32_16x16x32_bf16 v[46:49], v[168:171], v[210:213], v[46:49]
	v_mfma_f32_16x16x32_bf16 v[74:77], v[176:179], v[210:213], v[74:77]
	v_mfma_f32_16x16x32_bf16 v[34:37], v[172:175], v[188:191], v[34:37]
	v_mfma_f32_16x16x32_bf16 v[50:53], v[180:183], v[188:191], v[50:53]
	v_mfma_f32_16x16x32_bf16 v[38:41], v[172:175], v[196:199], v[38:41]
	v_mfma_f32_16x16x32_bf16 v[58:61], v[180:183], v[196:199], v[58:61]
	v_mfma_f32_16x16x32_bf16 v[42:45], v[172:175], v[206:209], v[42:45]
	v_mfma_f32_16x16x32_bf16 v[66:69], v[180:183], v[206:209], v[66:69]
	v_mfma_f32_16x16x32_bf16 v[46:49], v[172:175], v[214:217], v[46:49]
	v_mfma_f32_16x16x32_bf16 v[74:77], v[180:183], v[214:217], v[74:77]
	s_barrier
	s_mov_b32 m0, s56
	v_lshl_add_u64 v[218:219], s[24:25], 0, v[136:137]
	s_cselect_b32 s52, 0, s23
	s_cselect_b32 s53, 0, s22
	s_add_u32 s28, s24, 0x80000
	ds_read_b128 v[184:187], v150 offset:16384
	ds_read_b128 v[188:191], v150 offset:17408
	ds_read_b128 v[192:195], v150 offset:18432
	ds_read_b128 v[196:199], v150 offset:19456
	ds_read_b128 v[202:205], v150 offset:20480
	ds_read_b128 v[206:209], v150 offset:21504
	ds_read_b128 v[210:213], v150 offset:22528
	ds_read_b128 v[214:217], v150 offset:23552
	global_load_lds_dwordx4 v[218:219], off
	v_lshl_add_u64 v[220:221], s[24:25], 0, v[140:141]
	s_mov_b32 m0, s57
	s_addc_u32 s29, s25, 0
	s_add_i32 s54, s54, s33
	global_load_lds_dwordx4 v[220:221], off
	v_lshl_add_u64 v[222:223], s[28:29], 0, v[136:137]
	s_mov_b32 m0, s54
	s_nop 0
	global_load_lds_dwordx4 v[222:223], off
	v_lshl_add_u64 v[222:223], s[28:29], 0, v[140:141]
	s_add_i32 m0, s54, 0x2000
	s_and_b64 s[28:29], s[50:51], s[4:5]
	s_and_b64 s[28:29], s[28:29], exec
	s_cselect_b32 s28, s18, s10
	s_cselect_b32 s29, s19, s11
	s_add_u32 s28, s28, s53
	s_addc_u32 s29, s29, s52
	global_load_lds_dwordx4 v[222:223], off
	v_lshl_add_u64 v[222:223], s[28:29], 0, v[134:135]
	s_mov_b32 m0, s9
	v_lshl_add_u64 v[224:225], s[28:29], 0, v[138:139]
	global_load_lds_dwordx4 v[222:223], off
	s_mov_b32 m0, s38
	s_nop 0
	global_load_lds_dwordx4 v[224:225], off
	s_waitcnt vmcnt(8)
	s_waitcnt lgkmcnt(0)
	s_barrier
; #define PG8_STAGE_A(bufoff, base_, nx_, kb_, h_) do { if (GATHER) { if (nx_) PG8_STAGE_G(bufoff, kb_, goN, h_); else PG8_STAGE_G(bufoff, kb_, goC, h_); } \
;         else PG8_STAGE(bufoff, (base_) + (kb_) + (h_) * hstep, voffA); } while (0)
; #define PG8_LDA(dst, b, h) do { _Pragma("unroll") for (int m = 0; m < 4; ++m) _Pragma("unroll") for (int k = 0; k < 2; ++k) dst[m][k] = *(const LAS bf16x8*)(lds + PG8_SA(b, h) + aoff + m * 2048 + k * 1024); } while (0)
; #define PG8_LDB(dst, b, h) do { _Pragma("unroll") for (int n = 0; n < 2; ++n) _Pragma("unroll") for (int k = 0; k < 2; ++k) dst[n][k] = *(const LAS bf16x8*)(lds + PG8_SB(b, h) + boff + n * 2048 + k * 1024); } while (0)
; #define PG8_MMA(ai, bj, At, Bt) do { __builtin_amdgcn_s_setprio(1); _Pragma("unroll") for (int m = 0; m < 4; ++m) _Pragma("unroll") for (int n = 0; n < 2; ++n) _Pragma("unroll") for (int k = 0; k < 2; ++k) \
;         acc[ai][bj][m][n] = __builtin_amdgcn_mfma_f32_16x16x32_bf16(Bt[n][k], At[m][k], acc[ai][bj][m][n], 0, 0, 0); __builtin_amdgcn_s_setprio(0); } while (0)
; #define PG8_WAIT_V(n) asm volatile("s_waitcnt vmcnt(" #n ")" ::: "memory")
; #define PG8_WAIT_L(n) asm volatile("s_waitcnt lgkmcnt(" #n ")" ::: "memory")
; #define PG8_BAR __builtin_amdgcn_s_barrier()
; #define PG8_SCHED __builtin_amdgcn_sched_barrier(0)
; template <class Epi, class Sched, bool GATHER = false>
; __device__ __forceinline__ void gemm_phase(LAS unsigned char* lds, const Gemm g, const Sched& S, const Epi& E, const int tid) {
;     ...
;             PG8_WAIT_V(8); PG8_WAIT_L(0); PG8_BAR; PG8_MMA(1, 0, At, B0); PG8_MMA(1, 1, At, B1); PG8_BAR; PG8_SCHED;
;             PG8_LDB(B0, 1, 0); PG8_LDB(B1, 1, 1); PG8_SCHED; PG8_LDA(At, 1, 0); PG8_STAGE_A(PG8_SA(0, 1), (last ? nA : cA), last, kb2, 1);
;             PG8_WAIT_V(8); PG8_WAIT_L(0); PG8_BAR; PG8_MMA(0, 0, At, B0); PG8_MMA(0, 1, At, B1); PG8_BAR; PG8_SCHED;
	v_mfma_f32_16x16x32_bf16 v[54:57], v[152:155], v[184:187], v[54:57]
	v_mfma_f32_16x16x32_bf16 v[78:81], v[160:163], v[184:187], v[78:81]
	v_mfma_f32_16x16x32_bf16 v[62:65], v[152:155], v[192:195], v[62:65]
	v_mfma_f32_16x16x32_bf16 v[82:85], v[160:163], v[192:195], v[82:85]
	v_mfma_f32_16x16x32_bf16 v[70:73], v[152:155], v[202:205], v[70:73]
	v_mfma_f32_16x16x32_bf16 v[98:101], v[160:163], v[202:205], v[98:101]
	v_mfma_f32_16x16x32_bf16 v[90:93], v[152:155], v[210:213], v[90:93]
	v_mfma_f32_16x16x32_bf16 v[94:97], v[160:163], v[210:213], v[94:97]
	v_mfma_f32_16x16x32_bf16 v[54:57], v[156:159], v[188:191], v[54:57]
	v_mfma_f32_16x16x32_bf16 v[78:81], v[164:167], v[188:191], v[78:81]
	v_mfma_f32_16x16x32_bf16 v[62:65], v[156:159], v[196:199], v[62:65]
	v_mfma_f32_16x16x32_bf16 v[82:85], v[164:167], v[196:199], v[82:85]
	v_mfma_f32_16x16x32_bf16 v[70:73], v[156:159], v[206:209], v[70:73]
	v_mfma_f32_16x16x32_bf16 v[98:101], v[164:167], v[206:209], v[98:101]
	v_mfma_f32_16x16x32_bf16 v[90:93], v[156:159], v[214:217], v[90:93]
	v_mfma_f32_16x16x32_bf16 v[94:97], v[164:167], v[214:217], v[94:97]
	v_mfma_f32_16x16x32_bf16 v[114:117], v[168:171], v[184:187], v[114:117]
	v_mfma_f32_16x16x32_bf16 v[130:133], v[176:179], v[184:187], v[130:133]
	v_mfma_f32_16x16x32_bf16 v[110:113], v[168:171], v[192:195], v[110:113]
	v_mfma_f32_16x16x32_bf16 v[126:129], v[176:179], v[192:195], v[126:129]
	v_mfma_f32_16x16x32_bf16 v[106:109], v[168:171], v[202:205], v[106:109]
	v_mfma_f32_16x16x32_bf16 v[122:125], v[176:179], v[202:205], v[122:125]
	v_mfma_f32_16x16x32_bf16 v[102:105], v[168:171], v[210:213], v[102:105]
	v_mfma_f32_16x16x32_bf16 v[118:121], v[176:179], v[210:213], v[118:121]
	v_mfma_f32_16x16x32_bf16 v[114:117], v[172:175], v[188:191], v[114:117]
	v_mfma_f32_16x16x32_bf16 v[130:133], v[180:183], v[188:191], v[130:133]
	v_mfma_f32_16x16x32_bf16 v[110:113], v[172:175], v[196:199], v[110:113]
	v_mfma_f32_16x16x32_bf16 v[126:129], v[180:183], v[196:199], v[126:129]
	v_mfma_f32_16x16x32_bf16 v[106:109], v[172:175], v[206:209], v[106:109]
	v_mfma_f32_16x16x32_bf16 v[122:125], v[180:183], v[206:209], v[122:125]
	v_mfma_f32_16x16x32_bf16 v[102:105], v[172:175], v[214:217], v[102:105]
	v_mfma_f32_16x16x32_bf16 v[118:121], v[180:183], v[214:217], v[118:121]
	s_barrier
	s_add_i32 s50, 0, 0x18000
	v_add_u32_e32 v2, s50, v148
	s_add_i32 s51, 0, 0x1c000
	ds_read_b128 v[152:155], v2
	ds_read_b128 v[156:159], v2 offset:1024
	ds_read_b128 v[160:163], v2 offset:2048
	ds_read_b128 v[164:167], v2 offset:3072
	v_add_u32_e32 v2, s51, v148
	ds_read_b128 v[168:171], v2
	ds_read_b128 v[172:175], v2 offset:1024
	ds_read_b128 v[176:179], v2 offset:2048
	ds_read_b128 v[180:183], v2 offset:3072
	s_add_u32 s28, s28, 0x80000
	s_addc_u32 s29, s29, 0
	s_mov_b32 m0, s39
	v_lshl_add_u64 v[226:227], s[28:29], 0, v[134:135]
	ds_read_b128 v[184:187], v150 offset:32768
	ds_read_b128 v[188:191], v150 offset:33792
	ds_read_b128 v[192:195], v150 offset:34816
	ds_read_b128 v[196:199], v150 offset:35840
	ds_read_b128 v[202:205], v150 offset:36864
	ds_read_b128 v[206:209], v150 offset:37888
	ds_read_b128 v[210:213], v150 offset:38912
	ds_read_b128 v[214:217], v150 offset:39936
	global_load_lds_dwordx4 v[226:227], off
	v_lshl_add_u64 v[226:227], s[28:29], 0, v[138:139]
	s_mov_b32 m0, s40
	s_nop 0
	global_load_lds_dwordx4 v[226:227], off
	s_waitcnt vmcnt(8)
	s_waitcnt lgkmcnt(0)
	s_barrier
	v_mfma_f32_16x16x32_bf16 v[86:89], v[152:155], v[184:187], v[86:89]
	v_mfma_f32_16x16x32_bf16 v[18:21], v[160:163], v[184:187], v[18:21]
	v_mfma_f32_16x16x32_bf16 v[6:9], v[152:155], v[192:195], v[6:9]
	v_mfma_f32_16x16x32_bf16 v[22:25], v[160:163], v[192:195], v[22:25]
	v_mfma_f32_16x16x32_bf16 v[10:13], v[152:155], v[202:205], v[10:13]
	v_mfma_f32_16x16x32_bf16 v[26:29], v[160:163], v[202:205], v[26:29]
	v_mfma_f32_16x16x32_bf16 v[14:17], v[152:155], v[210:213], v[14:17]
	v_mfma_f32_16x16x32_bf16 v[30:33], v[160:163], v[210:213], v[30:33]
	v_mfma_f32_16x16x32_bf16 v[86:89], v[156:159], v[188:191], v[86:89]
	v_mfma_f32_16x16x32_bf16 v[18:21], v[164:167], v[188:191], v[18:21]
	v_mfma_f32_16x16x32_bf16 v[6:9], v[156:159], v[196:199], v[6:9]
	v_mfma_f32_16x16x32_bf16 v[22:25], v[164:167], v[196:199], v[22:25]
	v_mfma_f32_16x16x32_bf16 v[10:13], v[156:159], v[206:209], v[10:13]
	v_mfma_f32_16x16x32_bf16 v[26:29], v[164:167], v[206:209], v[26:29]
	v_mfma_f32_16x16x32_bf16 v[14:17], v[156:159], v[214:217], v[14:17]
	v_mfma_f32_16x16x32_bf16 v[30:33], v[164:167], v[214:217], v[30:33]
	v_mfma_f32_16x16x32_bf16 v[34:37], v[168:171], v[184:187], v[34:37]
	v_mfma_f32_16x16x32_bf16 v[50:53], v[176:179], v[184:187], v[50:53]
	v_mfma_f32_16x16x32_bf16 v[38:41], v[168:171], v[192:195], v[38:41]
	v_mfma_f32_16x16x32_bf16 v[58:61], v[176:179], v[192:195], v[58:61]
	v_mfma_f32_16x16x32_bf16 v[42:45], v[168:171], v[202:205], v[42:45]
	v_mfma_f32_16x16x32_bf16 v[66:69], v[176:179], v[202:205], v[66:69]
	v_mfma_f32_16x16x32_bf16 v[46:49], v[168:171], v[210:213], v[46:49]
	v_mfma_f32_16x16x32_bf16 v[74:77], v[176:179], v[210:213], v[74:77]
	v_mfma_f32_16x16x32_bf16 v[34:37], v[172:175], v[188:191], v[34:37]
	v_mfma_f32_16x16x32_bf16 v[50:53], v[180:183], v[188:191], v[50:53]
	v_mfma_f32_16x16x32_bf16 v[38:41], v[172:175], v[196:199], v[38:41]
	v_mfma_f32_16x16x32_bf16 v[58:61], v[180:183], v[196:199], v[58:61]
	v_mfma_f32_16x16x32_bf16 v[42:45], v[172:175], v[206:209], v[42:45]
	v_mfma_f32_16x16x32_bf16 v[66:69], v[180:183], v[206:209], v[66:69]
	v_mfma_f32_16x16x32_bf16 v[46:49], v[172:175], v[214:217], v[46:49]
	v_mfma_f32_16x16x32_bf16 v[74:77], v[180:183], v[214:217], v[74:77]
	s_barrier
; #define PG8_STAGE_A(bufoff, base_, nx_, kb_, h_) do { if (GATHER) { if (nx_) PG8_STAGE_G(bufoff, kb_, goN, h_); else PG8_STAGE_G(bufoff, kb_, goC, h_); } \
;         else PG8_STAGE(bufoff, (base_) + (kb_) + (h_) * hstep, voffA); } while (0)
; #define PG8_STAGE(bufoff, gbase, voff) do { _Pragma("unroll") for (int _i = 0; _i < 2; ++_i) \
;         __builtin_amdgcn_global_load_lds((const unsigned*)((const char*)(gbase) + (voff)[_i]), (LAS unsigned*)(lds + (bufoff) + ldsw + _i * 8192), 16, 0, 0); } while (0)
; #define PG8_LDA(dst, b, h) do { _Pragma("unroll") for (int m = 0; m < 4; ++m) _Pragma("unroll") for (int k = 0; k < 2; ++k) dst[m][k] = *(const LAS bf16x8*)(lds + PG8_SA(b, h) + aoff + m * 2048 + k * 1024); } while (0)
; #define PG8_MMA(ai, bj, At, Bt) do { __builtin_amdgcn_s_setprio(1); _Pragma("unroll") for (int m = 0; m < 4; ++m) _Pragma("unroll") for (int n = 0; n < 2; ++n) _Pragma("unroll") for (int k = 0; k < 2; ++k) \
;         acc[ai][bj][m][n] = __builtin_amdgcn_mfma_f32_16x16x32_bf16(Bt[n][k], At[m][k], acc[ai][bj][m][n], 0, 0, 0); __builtin_amdgcn_s_setprio(0); } while (0)
; #define PG8_WAIT_V(n) asm volatile("s_waitcnt vmcnt(" #n ")" ::: "memory")
; #define PG8_WAIT_L(n) asm volatile("s_waitcnt lgkmcnt(" #n ")" ::: "memory")
; #define PG8_BAR __builtin_amdgcn_s_barrier()
; #define PG8_SCHED __builtin_amdgcn_sched_barrier(0)
; template <class Epi, class Sched, bool GATHER = false>
; __device__ __forceinline__ void gemm_phase(LAS unsigned char* lds, const Gemm g, const Sched& S, const Epi& E, const int tid) {
;     ...
;             PG8_LDA(At, 1, 1); PG8_STAGE(PG8_SB(1, 0), b3, voffB); PG8_STAGE(PG8_SB(1, 1), b3 + hstep, voffB); PG8_STAGE_A(PG8_SA(1, 0), (last ? nA : cA), last, kb3, 0);
;             PG8_WAIT_V(8); PG8_WAIT_L(0); PG8_BAR; PG8_MMA(1, 0, At, B0); PG8_MMA(1, 1, At, B1); PG8_BAR; PG8_SCHED;
;     ...
;         }
;         if (wr == 0) PG8_BAR;
	s_add_i32 s28, s50, s33
	v_lshl_add_u64 v[218:219], v[218:219], 0, s[0:1]
	s_mov_b32 m0, s28
	ds_read_b128 v[184:187], v150 offset:49152
	ds_read_b128 v[188:191], v150 offset:50176
	ds_read_b128 v[192:195], v150 offset:51200
	ds_read_b128 v[196:199], v150 offset:52224
	ds_read_b128 v[202:205], v150 offset:53248
	ds_read_b128 v[206:209], v150 offset:54272
	ds_read_b128 v[210:213], v150 offset:55296
	ds_read_b128 v[214:217], v150 offset:56320
	global_load_lds_dwordx4 v[218:219], off
	s_add_i32 m0, s28, 0x2000
	s_add_u32 s24, s24, 0x80080
	v_lshl_add_u64 v[218:219], v[220:221], 0, s[0:1]
	s_addc_u32 s25, s25, 0
	s_add_i32 s28, s51, s33
	global_load_lds_dwordx4 v[218:219], off
	v_lshl_add_u64 v[218:219], s[24:25], 0, v[136:137]
	s_mov_b32 m0, s28
	s_nop 0
	global_load_lds_dwordx4 v[218:219], off
	v_lshl_add_u64 v[218:219], s[24:25], 0, v[140:141]
	s_add_i32 m0, s28, 0x2000
	s_nop 0
	global_load_lds_dwordx4 v[218:219], off
	v_lshl_add_u64 v[218:219], v[222:223], 0, s[0:1]
	s_mov_b32 m0, s42
	s_nop 0
	global_load_lds_dwordx4 v[218:219], off
	v_lshl_add_u64 v[218:219], v[224:225], 0, s[0:1]
	s_mov_b32 m0, s43
	s_nop 0
	global_load_lds_dwordx4 v[218:219], off
	s_waitcnt vmcnt(8)
	s_waitcnt lgkmcnt(0)
	s_barrier
	v_mfma_f32_16x16x32_bf16 v[54:57], v[152:155], v[184:187], v[54:57]
	v_mfma_f32_16x16x32_bf16 v[78:81], v[160:163], v[184:187], v[78:81]
	v_mfma_f32_16x16x32_bf16 v[62:65], v[152:155], v[192:195], v[62:65]
	v_mfma_f32_16x16x32_bf16 v[82:85], v[160:163], v[192:195], v[82:85]
	v_mfma_f32_16x16x32_bf16 v[70:73], v[152:155], v[202:205], v[70:73]
	v_mfma_f32_16x16x32_bf16 v[98:101], v[160:163], v[202:205], v[98:101]
	v_mfma_f32_16x16x32_bf16 v[90:93], v[152:155], v[210:213], v[90:93]
	v_mfma_f32_16x16x32_bf16 v[94:97], v[160:163], v[210:213], v[94:97]
	v_mfma_f32_16x16x32_bf16 v[54:57], v[156:159], v[188:191], v[54:57]
	v_mfma_f32_16x16x32_bf16 v[78:81], v[164:167], v[188:191], v[78:81]
	v_mfma_f32_16x16x32_bf16 v[62:65], v[156:159], v[196:199], v[62:65]
	v_mfma_f32_16x16x32_bf16 v[82:85], v[164:167], v[196:199], v[82:85]
	v_mfma_f32_16x16x32_bf16 v[70:73], v[156:159], v[206:209], v[70:73]
	v_mfma_f32_16x16x32_bf16 v[98:101], v[164:167], v[206:209], v[98:101]
	v_mfma_f32_16x16x32_bf16 v[90:93], v[156:159], v[214:217], v[90:93]
	v_mfma_f32_16x16x32_bf16 v[94:97], v[164:167], v[214:217], v[94:97]
	v_mfma_f32_16x16x32_bf16 v[114:117], v[168:171], v[184:187], v[114:117]
	v_mfma_f32_16x16x32_bf16 v[130:133], v[176:179], v[184:187], v[130:133]
	v_mfma_f32_16x16x32_bf16 v[110:113], v[168:171], v[192:195], v[110:113]
	v_mfma_f32_16x16x32_bf16 v[126:129], v[176:179], v[192:195], v[126:129]
	v_mfma_f32_16x16x32_bf16 v[106:109], v[168:171], v[202:205], v[106:109]
	v_mfma_f32_16x16x32_bf16 v[122:125], v[176:179], v[202:205], v[122:125]
	v_mfma_f32_16x16x32_bf16 v[102:105], v[168:171], v[210:213], v[102:105]
	v_mfma_f32_16x16x32_bf16 v[118:121], v[176:179], v[210:213], v[118:121]
	v_mfma_f32_16x16x32_bf16 v[114:117], v[172:175], v[188:191], v[114:117]
	v_mfma_f32_16x16x32_bf16 v[130:133], v[180:183], v[188:191], v[130:133]
	v_mfma_f32_16x16x32_bf16 v[110:113], v[172:175], v[196:199], v[110:113]
	v_mfma_f32_16x16x32_bf16 v[126:129], v[180:183], v[196:199], v[126:129]
	v_mfma_f32_16x16x32_bf16 v[106:109], v[172:175], v[206:209], v[106:109]
	v_mfma_f32_16x16x32_bf16 v[122:125], v[180:183], v[206:209], v[122:125]
	v_mfma_f32_16x16x32_bf16 v[102:105], v[172:175], v[214:217], v[102:105]
	v_mfma_f32_16x16x32_bf16 v[118:121], v[180:183], v[214:217], v[118:121]
	s_barrier
	s_add_i32 s49, s49, 2
	s_cmp_gt_u32 s49, 29
	s_mov_b64 s[28:29], s[22:23]
	s_cbranch_scc0 .LBB0_1128
	s_and_b64 vcc, exec, s[12:13]
	s_cbranch_vccz .LBB0_1131
	s_barrier

; #define PG8_STAGE_A(bufoff, base_, nx_, kb_, h_) do { if (GATHER) { if (nx_) PG8_STAGE_G(bufoff, kb_, goN, h_); else PG8_STAGE_G(bufoff, kb_, goC, h_); } \
;         else PG8_STAGE(bufoff, (base_) + (kb_) + (h_) * hstep, voffA); } while (0)
; #define PG8_STAGE(bufoff, gbase, voff) do { _Pragma("unroll") for (int _i = 0; _i < 2; ++_i) \
;         __builtin_amdgcn_global_load_lds((const unsigned*)((const char*)(gbase) + (voff)[_i]), (LAS unsigned*)(lds + (bufoff) + ldsw + _i * 8192), 16, 0, 0); } while (0)
; #define PG8_LDA(dst, b, h) do { _Pragma("unroll") for (int m = 0; m < 4; ++m) _Pragma("unroll") for (int k = 0; k < 2; ++k) dst[m][k] = *(const LAS bf16x8*)(lds + PG8_SA(b, h) + aoff + m * 2048 + k * 1024); } while (0)
; #define PG8_LDB(dst, b, h) do { _Pragma("unroll") for (int n = 0; n < 2; ++n) _Pragma("unroll") for (int k = 0; k < 2; ++k) dst[n][k] = *(const LAS bf16x8*)(lds + PG8_SB(b, h) + boff + n * 2048 + k * 1024); } while (0)
; #define PG8_MMA(ai, bj, At, Bt) do { __builtin_amdgcn_s_setprio(1); _Pragma("unroll") for (int m = 0; m < 4; ++m) _Pragma("unroll") for (int n = 0; n < 2; ++n) _Pragma("unroll") for (int k = 0; k < 2; ++k) \
;         acc[ai][bj][m][n] = __builtin_amdgcn_mfma_f32_16x16x32_bf16(Bt[n][k], At[m][k], acc[ai][bj][m][n], 0, 0, 0); __builtin_amdgcn_s_setprio(0); } while (0)
; #define PG8_WAIT_V(n) asm volatile("s_waitcnt vmcnt(" #n ")" ::: "memory")
; #define PG8_WAIT_L(n) asm volatile("s_waitcnt lgkmcnt(" #n ")" ::: "memory")
; #define PG8_BAR __builtin_amdgcn_s_barrier()
; #define PG8_SCHED __builtin_amdgcn_sched_barrier(0)
; template <class Epi, class Sched, bool GATHER = false>
; __device__ __forceinline__ void gemm_phase(LAS unsigned char* lds, const Gemm g, const Sched& S, const Epi& E, const int tid) {
;     ...
;             PG8_LDB(B0, 0, 0); PG8_LDB(B1, 0, 1); PG8_SCHED; PG8_LDA(At, 0, 0); PG8_STAGE_A(PG8_SA(1, 1), cA, false, kb1, 1);
;             PG8_WAIT_V(8); PG8_WAIT_L(0); PG8_BAR; PG8_MMA(0, 0, At, B0); PG8_MMA(0, 1, At, B1); PG8_BAR; PG8_SCHED;
;             PG8_LDA(At, 0, 1); PG8_STAGE(PG8_SB(0, 0), b2, voffB); PG8_STAGE(PG8_SB(0, 1), b2 + hstep, voffB); PG8_STAGE_A(PG8_SA(0, 0), (last ? nA : cA), last, kb2, 0);
;             PG8_WAIT_V(8); PG8_WAIT_L(0); PG8_BAR; PG8_MMA(1, 0, At, B0); PG8_MMA(1, 1, At, B1); PG8_BAR; PG8_SCHED;
.LBB0_1367:
	s_add_u32 s62, s59, s40
	s_addc_u32 s63, s60, s41
	s_add_u32 s36, s40, 0x100
	s_addc_u32 s37, s41, 0
	s_cmp_eq_u32 s61, 28
	s_cselect_b64 s[42:43], -1, 0
	s_and_b64 s[38:39], s[42:43], exec
	s_cselect_b32 s39, s21, s63
	s_cselect_b32 s38, s23, s62
	s_cselect_b32 s62, 0, s36
	s_add_i32 s63, 0, 0x10000
	v_add_u32_e32 v2, s63, v135
	s_add_i32 s64, 0, 0x14000
	ds_read_b128 v[152:155], v2
	ds_read_b128 v[156:159], v2 offset:1024
	ds_read_b128 v[160:163], v2 offset:2048
	ds_read_b128 v[164:167], v2 offset:3072
	v_add_u32_e32 v2, s64, v135
	ds_read_b128 v[168:171], v2
	ds_read_b128 v[172:175], v2 offset:1024
	ds_read_b128 v[176:179], v2 offset:2048
	ds_read_b128 v[180:183], v2 offset:3072
	v_lshl_add_u64 v[218:219], v[4:5], 0, s[40:41]
	s_add_i32 m0, s31, 0xc000
	ds_read_b128 v[184:187], v151
	ds_read_b128 v[188:191], v151 offset:1024
	ds_read_b128 v[192:195], v151 offset:2048
	ds_read_b128 v[196:199], v151 offset:3072
	ds_read_b128 v[202:205], v151 offset:4096
	ds_read_b128 v[206:209], v151 offset:5120
	ds_read_b128 v[210:213], v151 offset:6144
	ds_read_b128 v[214:217], v151 offset:7168
	global_load_lds_dwordx4 v[218:219], off
	v_lshl_add_u64 v[218:219], v[148:149], 0, s[40:41]
	s_add_i32 m0, s31, 0xe000
	s_nop 0
	global_load_lds_dwordx4 v[218:219], off
	s_waitcnt vmcnt(8)
	s_waitcnt lgkmcnt(0)
	s_barrier
	v_mfma_f32_16x16x32_bf16 v[122:125], v[152:155], v[184:187], v[122:125]
	v_mfma_f32_16x16x32_bf16 v[74:77], v[160:163], v[184:187], v[74:77]
	v_mfma_f32_16x16x32_bf16 v[58:61], v[152:155], v[192:195], v[58:61]
	v_mfma_f32_16x16x32_bf16 v[50:53], v[160:163], v[192:195], v[50:53]
	v_mfma_f32_16x16x32_bf16 v[38:41], v[152:155], v[202:205], v[38:41]
	v_mfma_f32_16x16x32_bf16 v[34:37], v[160:163], v[202:205], v[34:37]
	v_mfma_f32_16x16x32_bf16 v[22:25], v[152:155], v[210:213], v[22:25]
	v_mfma_f32_16x16x32_bf16 v[18:21], v[160:163], v[210:213], v[18:21]
	v_mfma_f32_16x16x32_bf16 v[122:125], v[156:159], v[188:191], v[122:125]
	v_mfma_f32_16x16x32_bf16 v[74:77], v[164:167], v[188:191], v[74:77]
	v_mfma_f32_16x16x32_bf16 v[58:61], v[156:159], v[196:199], v[58:61]
	v_mfma_f32_16x16x32_bf16 v[50:53], v[164:167], v[196:199], v[50:53]
	v_mfma_f32_16x16x32_bf16 v[38:41], v[156:159], v[206:209], v[38:41]
	v_mfma_f32_16x16x32_bf16 v[34:37], v[164:167], v[206:209], v[34:37]
	v_mfma_f32_16x16x32_bf16 v[22:25], v[156:159], v[214:217], v[22:25]
	v_mfma_f32_16x16x32_bf16 v[18:21], v[164:167], v[214:217], v[18:21]
	v_mfma_f32_16x16x32_bf16 v[106:109], v[168:171], v[184:187], v[106:109]
	v_mfma_f32_16x16x32_bf16 v[110:113], v[176:179], v[184:187], v[110:113]
	v_mfma_f32_16x16x32_bf16 v[90:93], v[168:171], v[192:195], v[90:93]
	v_mfma_f32_16x16x32_bf16 v[94:97], v[176:179], v[192:195], v[94:97]
	v_mfma_f32_16x16x32_bf16 v[66:69], v[168:171], v[202:205], v[66:69]
	v_mfma_f32_16x16x32_bf16 v[70:73], v[176:179], v[202:205], v[70:73]
	v_mfma_f32_16x16x32_bf16 v[42:45], v[168:171], v[210:213], v[42:45]
	v_mfma_f32_16x16x32_bf16 v[46:49], v[176:179], v[210:213], v[46:49]
	v_mfma_f32_16x16x32_bf16 v[106:109], v[172:175], v[188:191], v[106:109]
	v_mfma_f32_16x16x32_bf16 v[110:113], v[180:183], v[188:191], v[110:113]
	v_mfma_f32_16x16x32_bf16 v[90:93], v[172:175], v[196:199], v[90:93]
	v_mfma_f32_16x16x32_bf16 v[94:97], v[180:183], v[196:199], v[94:97]
	v_mfma_f32_16x16x32_bf16 v[66:69], v[172:175], v[206:209], v[66:69]
	v_mfma_f32_16x16x32_bf16 v[70:73], v[180:183], v[206:209], v[70:73]
	v_mfma_f32_16x16x32_bf16 v[42:45], v[172:175], v[214:217], v[42:45]
	v_mfma_f32_16x16x32_bf16 v[46:49], v[180:183], v[214:217], v[46:49]
	s_barrier
	s_add_i32 s40, s63, s50
	v_lshl_add_u64 v[218:219], s[38:39], 0, v[140:141]
	s_mov_b32 m0, s40
	ds_read_b128 v[184:187], v151 offset:16384
	ds_read_b128 v[188:191], v151 offset:17408
	ds_read_b128 v[192:195], v151 offset:18432
	ds_read_b128 v[196:199], v151 offset:19456
	ds_read_b128 v[202:205], v151 offset:20480
	ds_read_b128 v[206:209], v151 offset:21504
	ds_read_b128 v[210:213], v151 offset:22528
	ds_read_b128 v[214:217], v151 offset:23552
	global_load_lds_dwordx4 v[218:219], off
	s_add_i32 m0, s40, 0x2000
	s_add_u32 s40, s38, 0x80000
	v_lshl_add_u64 v[220:221], s[38:39], 0, v[136:137]
	s_addc_u32 s41, s39, 0
	s_add_i32 s63, s64, s50
	global_load_lds_dwordx4 v[220:221], off
	v_lshl_add_u64 v[222:223], s[40:41], 0, v[140:141]
	s_mov_b32 m0, s63
	s_nop 0
	global_load_lds_dwordx4 v[222:223], off
	v_lshl_add_u64 v[222:223], s[40:41], 0, v[136:137]
	s_add_i32 m0, s63, 0x2000
	s_and_b64 s[40:41], s[8:9], s[42:43]
	s_and_b64 s[40:41], s[40:41], exec
	s_cselect_b32 s40, s24, s34
	s_cselect_b32 s41, s25, s35
	s_add_u32 s40, s40, s62
	s_addc_u32 s41, s41, 0
	global_load_lds_dwordx4 v[222:223], off
	v_lshl_add_u64 v[222:223], s[40:41], 0, v[142:143]
	s_mov_b32 m0, s31
	v_lshl_add_u64 v[224:225], s[40:41], 0, v[138:139]
	global_load_lds_dwordx4 v[222:223], off
	s_mov_b32 m0, s52
	s_nop 0
	global_load_lds_dwordx4 v[224:225], off
	s_waitcnt vmcnt(8)
	s_waitcnt lgkmcnt(0)
	s_barrier
; #define PG8_STAGE_A(bufoff, base_, nx_, kb_, h_) do { if (GATHER) { if (nx_) PG8_STAGE_G(bufoff, kb_, goN, h_); else PG8_STAGE_G(bufoff, kb_, goC, h_); } \
;         else PG8_STAGE(bufoff, (base_) + (kb_) + (h_) * hstep, voffA); } while (0)
; #define PG8_LDA(dst, b, h) do { _Pragma("unroll") for (int m = 0; m < 4; ++m) _Pragma("unroll") for (int k = 0; k < 2; ++k) dst[m][k] = *(const LAS bf16x8*)(lds + PG8_SA(b, h) + aoff + m * 2048 + k * 1024); } while (0)
; #define PG8_LDB(dst, b, h) do { _Pragma("unroll") for (int n = 0; n < 2; ++n) _Pragma("unroll") for (int k = 0; k < 2; ++k) dst[n][k] = *(const LAS bf16x8*)(lds + PG8_SB(b, h) + boff + n * 2048 + k * 1024); } while (0)
; #define PG8_MMA(ai, bj, At, Bt) do { __builtin_amdgcn_s_setprio(1); _Pragma("unroll") for (int m = 0; m < 4; ++m) _Pragma("unroll") for (int n = 0; n < 2; ++n) _Pragma("unroll") for (int k = 0; k < 2; ++k) \
;         acc[ai][bj][m][n] = __builtin_amdgcn_mfma_f32_16x16x32_bf16(Bt[n][k], At[m][k], acc[ai][bj][m][n], 0, 0, 0); __builtin_amdgcn_s_setprio(0); } while (0)
; #define PG8_WAIT_V(n) asm volatile("s_waitcnt vmcnt(" #n ")" ::: "memory")
; #define PG8_WAIT_L(n) asm volatile("s_waitcnt lgkmcnt(" #n ")" ::: "memory")
; #define PG8_BAR __builtin_amdgcn_s_barrier()
; #define PG8_SCHED __builtin_amdgcn_sched_barrier(0)
; template <class Epi, class Sched, bool GATHER = false>
; __device__ __forceinline__ void gemm_phase(LAS unsigned char* lds, const Gemm g, const Sched& S, const Epi& E, const int tid) {
;     ...
;             PG8_WAIT_V(8); PG8_WAIT_L(0); PG8_BAR; PG8_MMA(1, 0, At, B0); PG8_MMA(1, 1, At, B1); PG8_BAR; PG8_SCHED;
;             PG8_LDB(B0, 1, 0); PG8_LDB(B1, 1, 1); PG8_SCHED; PG8_LDA(At, 1, 0); PG8_STAGE_A(PG8_SA(0, 1), (last ? nA : cA), last, kb2, 1);
;             PG8_WAIT_V(8); PG8_WAIT_L(0); PG8_BAR; PG8_MMA(0, 0, At, B0); PG8_MMA(0, 1, At, B1); PG8_BAR; PG8_SCHED;
	v_mfma_f32_16x16x32_bf16 v[30:33], v[152:155], v[184:187], v[30:33]
	v_mfma_f32_16x16x32_bf16 v[26:29], v[160:163], v[184:187], v[26:29]
	v_mfma_f32_16x16x32_bf16 v[14:17], v[152:155], v[192:195], v[14:17]
	v_mfma_f32_16x16x32_bf16 v[10:13], v[160:163], v[192:195], v[10:13]
	v_mfma_f32_16x16x32_bf16 v[6:9], v[152:155], v[202:205], v[6:9]
	v_mfma_f32_16x16x32_bf16 v[78:81], v[160:163], v[202:205], v[78:81]
	v_mfma_f32_16x16x32_bf16 v[62:65], v[152:155], v[210:213], v[62:65]
	v_mfma_f32_16x16x32_bf16 v[54:57], v[160:163], v[210:213], v[54:57]
	v_mfma_f32_16x16x32_bf16 v[30:33], v[156:159], v[188:191], v[30:33]
	v_mfma_f32_16x16x32_bf16 v[26:29], v[164:167], v[188:191], v[26:29]
	v_mfma_f32_16x16x32_bf16 v[14:17], v[156:159], v[196:199], v[14:17]
	v_mfma_f32_16x16x32_bf16 v[10:13], v[164:167], v[196:199], v[10:13]
	v_mfma_f32_16x16x32_bf16 v[6:9], v[156:159], v[206:209], v[6:9]
	v_mfma_f32_16x16x32_bf16 v[78:81], v[164:167], v[206:209], v[78:81]
	v_mfma_f32_16x16x32_bf16 v[62:65], v[156:159], v[214:217], v[62:65]
	v_mfma_f32_16x16x32_bf16 v[54:57], v[164:167], v[214:217], v[54:57]
	v_mfma_f32_16x16x32_bf16 v[130:133], v[168:171], v[184:187], v[130:133]
	v_mfma_f32_16x16x32_bf16 v[126:129], v[176:179], v[184:187], v[126:129]
	v_mfma_f32_16x16x32_bf16 v[118:121], v[168:171], v[192:195], v[118:121]
	v_mfma_f32_16x16x32_bf16 v[114:117], v[176:179], v[192:195], v[114:117]
	v_mfma_f32_16x16x32_bf16 v[102:105], v[168:171], v[202:205], v[102:105]
	v_mfma_f32_16x16x32_bf16 v[98:101], v[176:179], v[202:205], v[98:101]
	v_mfma_f32_16x16x32_bf16 v[86:89], v[168:171], v[210:213], v[86:89]
	v_mfma_f32_16x16x32_bf16 v[82:85], v[176:179], v[210:213], v[82:85]
	v_mfma_f32_16x16x32_bf16 v[130:133], v[172:175], v[188:191], v[130:133]
	v_mfma_f32_16x16x32_bf16 v[126:129], v[180:183], v[188:191], v[126:129]
	v_mfma_f32_16x16x32_bf16 v[118:121], v[172:175], v[196:199], v[118:121]
	v_mfma_f32_16x16x32_bf16 v[114:117], v[180:183], v[196:199], v[114:117]
	v_mfma_f32_16x16x32_bf16 v[102:105], v[172:175], v[206:209], v[102:105]
	v_mfma_f32_16x16x32_bf16 v[98:101], v[180:183], v[206:209], v[98:101]
	v_mfma_f32_16x16x32_bf16 v[86:89], v[172:175], v[214:217], v[86:89]
	v_mfma_f32_16x16x32_bf16 v[82:85], v[180:183], v[214:217], v[82:85]
	s_barrier
	s_add_i32 s42, 0, 0x18000
	v_add_u32_e32 v2, s42, v135
	s_add_i32 s43, 0, 0x1c000
	ds_read_b128 v[152:155], v2
	ds_read_b128 v[156:159], v2 offset:1024
	ds_read_b128 v[160:163], v2 offset:2048
	ds_read_b128 v[164:167], v2 offset:3072
	v_add_u32_e32 v2, s43, v135
	ds_read_b128 v[168:171], v2
	ds_read_b128 v[172:175], v2 offset:1024
	ds_read_b128 v[176:179], v2 offset:2048
	ds_read_b128 v[180:183], v2 offset:3072
	s_add_u32 s40, s40, 0x80000
	s_addc_u32 s41, s41, 0
	s_mov_b32 m0, s53
	v_lshl_add_u64 v[226:227], s[40:41], 0, v[142:143]
	ds_read_b128 v[184:187], v151 offset:32768
	ds_read_b128 v[188:191], v151 offset:33792
	ds_read_b128 v[192:195], v151 offset:34816
	ds_read_b128 v[196:199], v151 offset:35840
	ds_read_b128 v[202:205], v151 offset:36864
	ds_read_b128 v[206:209], v151 offset:37888
	ds_read_b128 v[210:213], v151 offset:38912
	ds_read_b128 v[214:217], v151 offset:39936
	global_load_lds_dwordx4 v[226:227], off
	v_lshl_add_u64 v[226:227], s[40:41], 0, v[138:139]
	s_mov_b32 m0, s54
	s_nop 0
	global_load_lds_dwordx4 v[226:227], off
	s_waitcnt vmcnt(8)
	s_waitcnt lgkmcnt(0)
	s_barrier
	v_mfma_f32_16x16x32_bf16 v[122:125], v[152:155], v[184:187], v[122:125]
	v_mfma_f32_16x16x32_bf16 v[74:77], v[160:163], v[184:187], v[74:77]
	v_mfma_f32_16x16x32_bf16 v[58:61], v[152:155], v[192:195], v[58:61]
	v_mfma_f32_16x16x32_bf16 v[50:53], v[160:163], v[192:195], v[50:53]
	v_mfma_f32_16x16x32_bf16 v[38:41], v[152:155], v[202:205], v[38:41]
	v_mfma_f32_16x16x32_bf16 v[34:37], v[160:163], v[202:205], v[34:37]
	v_mfma_f32_16x16x32_bf16 v[22:25], v[152:155], v[210:213], v[22:25]
	v_mfma_f32_16x16x32_bf16 v[18:21], v[160:163], v[210:213], v[18:21]
	v_mfma_f32_16x16x32_bf16 v[122:125], v[156:159], v[188:191], v[122:125]
	v_mfma_f32_16x16x32_bf16 v[74:77], v[164:167], v[188:191], v[74:77]
	v_mfma_f32_16x16x32_bf16 v[58:61], v[156:159], v[196:199], v[58:61]
	v_mfma_f32_16x16x32_bf16 v[50:53], v[164:167], v[196:199], v[50:53]
	v_mfma_f32_16x16x32_bf16 v[38:41], v[156:159], v[206:209], v[38:41]
	v_mfma_f32_16x16x32_bf16 v[34:37], v[164:167], v[206:209], v[34:37]
	v_mfma_f32_16x16x32_bf16 v[22:25], v[156:159], v[214:217], v[22:25]
	v_mfma_f32_16x16x32_bf16 v[18:21], v[164:167], v[214:217], v[18:21]
	v_mfma_f32_16x16x32_bf16 v[106:109], v[168:171], v[184:187], v[106:109]
	v_mfma_f32_16x16x32_bf16 v[110:113], v[176:179], v[184:187], v[110:113]
	v_mfma_f32_16x16x32_bf16 v[90:93], v[168:171], v[192:195], v[90:93]
	v_mfma_f32_16x16x32_bf16 v[94:97], v[176:179], v[192:195], v[94:97]
	v_mfma_f32_16x16x32_bf16 v[66:69], v[168:171], v[202:205], v[66:69]
	v_mfma_f32_16x16x32_bf16 v[70:73], v[176:179], v[202:205], v[70:73]
	v_mfma_f32_16x16x32_bf16 v[42:45], v[168:171], v[210:213], v[42:45]
	v_mfma_f32_16x16x32_bf16 v[46:49], v[176:179], v[210:213], v[46:49]
	v_mfma_f32_16x16x32_bf16 v[106:109], v[172:175], v[188:191], v[106:109]
	v_mfma_f32_16x16x32_bf16 v[110:113], v[180:183], v[188:191], v[110:113]
	v_mfma_f32_16x16x32_bf16 v[90:93], v[172:175], v[196:199], v[90:93]
	v_mfma_f32_16x16x32_bf16 v[94:97], v[180:183], v[196:199], v[94:97]
	v_mfma_f32_16x16x32_bf16 v[66:69], v[172:175], v[206:209], v[66:69]
	v_mfma_f32_16x16x32_bf16 v[70:73], v[180:183], v[206:209], v[70:73]
	v_mfma_f32_16x16x32_bf16 v[42:45], v[172:175], v[214:217], v[42:45]
	v_mfma_f32_16x16x32_bf16 v[46:49], v[180:183], v[214:217], v[46:49]
	s_barrier
; #define PG8_STAGE_A(bufoff, base_, nx_, kb_, h_) do { if (GATHER) { if (nx_) PG8_STAGE_G(bufoff, kb_, goN, h_); else PG8_STAGE_G(bufoff, kb_, goC, h_); } \
;         else PG8_STAGE(bufoff, (base_) + (kb_) + (h_) * hstep, voffA); } while (0)
; #define PG8_STAGE(bufoff, gbase, voff) do { _Pragma("unroll") for (int _i = 0; _i < 2; ++_i) \
;         __builtin_amdgcn_global_load_lds((const unsigned*)((const char*)(gbase) + (voff)[_i]), (LAS unsigned*)(lds + (bufoff) + ldsw + _i * 8192), 16, 0, 0); } while (0)
; #define PG8_LDA(dst, b, h) do { _Pragma("unroll") for (int m = 0; m < 4; ++m) _Pragma("unroll") for (int k = 0; k < 2; ++k) dst[m][k] = *(const LAS bf16x8*)(lds + PG8_SA(b, h) + aoff + m * 2048 + k * 1024); } while (0)
; #define PG8_MMA(ai, bj, At, Bt) do { __builtin_amdgcn_s_setprio(1); _Pragma("unroll") for (int m = 0; m < 4; ++m) _Pragma("unroll") for (int n = 0; n < 2; ++n) _Pragma("unroll") for (int k = 0; k < 2; ++k) \
;         acc[ai][bj][m][n] = __builtin_amdgcn_mfma_f32_16x16x32_bf16(Bt[n][k], At[m][k], acc[ai][bj][m][n], 0, 0, 0); __builtin_amdgcn_s_setprio(0); } while (0)
; #define PG8_WAIT_V(n) asm volatile("s_waitcnt vmcnt(" #n ")" ::: "memory")
; #define PG8_WAIT_L(n) asm volatile("s_waitcnt lgkmcnt(" #n ")" ::: "memory")
; #define PG8_BAR __builtin_amdgcn_s_barrier()
; #define PG8_SCHED __builtin_amdgcn_sched_barrier(0)
; template <class Epi, class Sched, bool GATHER = false>
; __device__ __forceinline__ void gemm_phase(LAS unsigned char* lds, const Gemm g, const Sched& S, const Epi& E, const int tid) {
;     ...
;             PG8_LDA(At, 1, 1); PG8_STAGE(PG8_SB(1, 0), b3, voffB); PG8_STAGE(PG8_SB(1, 1), b3 + hstep, voffB); PG8_STAGE_A(PG8_SA(1, 0), (last ? nA : cA), last, kb3, 0);
;             PG8_WAIT_V(8); PG8_WAIT_L(0); PG8_BAR; PG8_MMA(1, 0, At, B0); PG8_MMA(1, 1, At, B1); PG8_BAR; PG8_SCHED;
;     ...
;         }
;         if (wr == 0) PG8_BAR;
	s_add_i32 s40, s42, s50
	v_lshl_add_u64 v[218:219], v[218:219], 0, s[0:1]
	s_mov_b32 m0, s40
	ds_read_b128 v[184:187], v151 offset:49152
	ds_read_b128 v[188:191], v151 offset:50176
	ds_read_b128 v[192:195], v151 offset:51200
	ds_read_b128 v[196:199], v151 offset:52224
	ds_read_b128 v[202:205], v151 offset:53248
	ds_read_b128 v[206:209], v151 offset:54272
	ds_read_b128 v[210:213], v151 offset:55296
	ds_read_b128 v[214:217], v151 offset:56320
	global_load_lds_dwordx4 v[218:219], off
	s_add_i32 m0, s40, 0x2000
	s_add_u32 s38, s38, 0x80080
	v_lshl_add_u64 v[218:219], v[220:221], 0, s[0:1]
	s_addc_u32 s39, s39, 0
	s_add_i32 s40, s43, s50
	global_load_lds_dwordx4 v[218:219], off
	v_lshl_add_u64 v[218:219], s[38:39], 0, v[140:141]
	s_mov_b32 m0, s40
	s_nop 0
	global_load_lds_dwordx4 v[218:219], off
	v_lshl_add_u64 v[218:219], s[38:39], 0, v[136:137]
	s_add_i32 m0, s40, 0x2000
	s_nop 0
	global_load_lds_dwordx4 v[218:219], off
	v_lshl_add_u64 v[218:219], v[222:223], 0, s[0:1]
	s_mov_b32 m0, s33
	s_nop 0
	global_load_lds_dwordx4 v[218:219], off
	v_lshl_add_u64 v[218:219], v[224:225], 0, s[0:1]
	s_mov_b32 m0, s55
	s_nop 0
	global_load_lds_dwordx4 v[218:219], off
	s_waitcnt vmcnt(8)
	s_waitcnt lgkmcnt(0)
	s_barrier
	v_mfma_f32_16x16x32_bf16 v[30:33], v[152:155], v[184:187], v[30:33]
	v_mfma_f32_16x16x32_bf16 v[26:29], v[160:163], v[184:187], v[26:29]
	v_mfma_f32_16x16x32_bf16 v[14:17], v[152:155], v[192:195], v[14:17]
	v_mfma_f32_16x16x32_bf16 v[10:13], v[160:163], v[192:195], v[10:13]
	v_mfma_f32_16x16x32_bf16 v[6:9], v[152:155], v[202:205], v[6:9]
	v_mfma_f32_16x16x32_bf16 v[78:81], v[160:163], v[202:205], v[78:81]
	v_mfma_f32_16x16x32_bf16 v[62:65], v[152:155], v[210:213], v[62:65]
	v_mfma_f32_16x16x32_bf16 v[54:57], v[160:163], v[210:213], v[54:57]
	v_mfma_f32_16x16x32_bf16 v[30:33], v[156:159], v[188:191], v[30:33]
	v_mfma_f32_16x16x32_bf16 v[26:29], v[164:167], v[188:191], v[26:29]
	v_mfma_f32_16x16x32_bf16 v[14:17], v[156:159], v[196:199], v[14:17]
	v_mfma_f32_16x16x32_bf16 v[10:13], v[164:167], v[196:199], v[10:13]
	v_mfma_f32_16x16x32_bf16 v[6:9], v[156:159], v[206:209], v[6:9]
	v_mfma_f32_16x16x32_bf16 v[78:81], v[164:167], v[206:209], v[78:81]
	v_mfma_f32_16x16x32_bf16 v[62:65], v[156:159], v[214:217], v[62:65]
	v_mfma_f32_16x16x32_bf16 v[54:57], v[164:167], v[214:217], v[54:57]
	v_mfma_f32_16x16x32_bf16 v[130:133], v[168:171], v[184:187], v[130:133]
	v_mfma_f32_16x16x32_bf16 v[126:129], v[176:179], v[184:187], v[126:129]
	v_mfma_f32_16x16x32_bf16 v[118:121], v[168:171], v[192:195], v[118:121]
	v_mfma_f32_16x16x32_bf16 v[114:117], v[176:179], v[192:195], v[114:117]
	v_mfma_f32_16x16x32_bf16 v[102:105], v[168:171], v[202:205], v[102:105]
	v_mfma_f32_16x16x32_bf16 v[98:101], v[176:179], v[202:205], v[98:101]
	v_mfma_f32_16x16x32_bf16 v[86:89], v[168:171], v[210:213], v[86:89]
	v_mfma_f32_16x16x32_bf16 v[82:85], v[176:179], v[210:213], v[82:85]
	v_mfma_f32_16x16x32_bf16 v[130:133], v[172:175], v[188:191], v[130:133]
	v_mfma_f32_16x16x32_bf16 v[126:129], v[180:183], v[188:191], v[126:129]
	v_mfma_f32_16x16x32_bf16 v[118:121], v[172:175], v[196:199], v[118:121]
	v_mfma_f32_16x16x32_bf16 v[114:117], v[180:183], v[196:199], v[114:117]
	v_mfma_f32_16x16x32_bf16 v[102:105], v[172:175], v[206:209], v[102:105]
	v_mfma_f32_16x16x32_bf16 v[98:101], v[180:183], v[206:209], v[98:101]
	v_mfma_f32_16x16x32_bf16 v[86:89], v[172:175], v[214:217], v[86:89]
	v_mfma_f32_16x16x32_bf16 v[82:85], v[180:183], v[214:217], v[82:85]
	s_barrier
	s_add_i32 s61, s61, 2
	s_cmp_gt_u32 s61, 29
	s_mov_b64 s[40:41], s[36:37]
	s_cbranch_scc0 .LBB0_1367
	s_and_b64 vcc, exec, s[16:17]
	s_cbranch_vccz .LBB0_1370
	s_barrier

; #define PG8_STAGE_A(bufoff, base_, nx_, kb_, h_) do { if (GATHER) { if (nx_) PG8_STAGE_G(bufoff, kb_, goN, h_); else PG8_STAGE_G(bufoff, kb_, goC, h_); } \
;         else PG8_STAGE(bufoff, (base_) + (kb_) + (h_) * hstep, voffA); } while (0)
; #define PG8_LDA(dst, b, h) do { _Pragma("unroll") for (int m = 0; m < 4; ++m) _Pragma("unroll") for (int k = 0; k < 2; ++k) dst[m][k] = *(const LAS bf16x8*)(lds + PG8_SA(b, h) + aoff + m * 2048 + k * 1024); } while (0)
; #define PG8_LDB(dst, b, h) do { _Pragma("unroll") for (int n = 0; n < 2; ++n) _Pragma("unroll") for (int k = 0; k < 2; ++k) dst[n][k] = *(const LAS bf16x8*)(lds + PG8_SB(b, h) + boff + n * 2048 + k * 1024); } while (0)
; #define PG8_MMA(ai, bj, At, Bt) do { __builtin_amdgcn_s_setprio(1); _Pragma("unroll") for (int m = 0; m < 4; ++m) _Pragma("unroll") for (int n = 0; n < 2; ++n) _Pragma("unroll") for (int k = 0; k < 2; ++k) \
;         acc[ai][bj][m][n] = __builtin_amdgcn_mfma_f32_16x16x32_bf16(Bt[n][k], At[m][k], acc[ai][bj][m][n], 0, 0, 0); __builtin_amdgcn_s_setprio(0); } while (0)
; #define PG8_WAIT_V(n) asm volatile("s_waitcnt vmcnt(" #n ")" ::: "memory")
; #define PG8_WAIT_L(n) asm volatile("s_waitcnt lgkmcnt(" #n ")" ::: "memory")
; #define PG8_BAR __builtin_amdgcn_s_barrier()
; #define PG8_SCHED __builtin_amdgcn_sched_barrier(0)
; template <class Epi, class Sched, bool GATHER = false>
; __device__ __forceinline__ void gemm_phase(LAS unsigned char* lds, const Gemm g, const Sched& S, const Epi& E, const int tid) {
;     ...
;             PG8_LDB(B0, 0, 0); PG8_LDB(B1, 0, 1); PG8_SCHED; PG8_LDA(At, 0, 0); PG8_STAGE_A(PG8_SA(1, 1), cA, false, kb1, 1);
;             PG8_WAIT_V(8); PG8_WAIT_L(0); PG8_BAR; PG8_MMA(0, 0, At, B0); PG8_MMA(0, 1, At, B1); PG8_BAR; PG8_SCHED;
.LBB0_1397:
	s_add_u32 s30, s36, 0x100
	s_addc_u32 s31, s37, 0
	s_and_b64 s[72:73], s[10:11], exec
	s_cselect_b32 s71, 0, s30
	s_add_i32 s72, 0, 0x10000
	v_add_u32_e32 v2, s72, v219
	s_add_i32 s73, 0, 0x14000
	ds_read_b128 v[134:137], v2
	ds_read_b128 v[138:141], v2 offset:1024
	ds_read_b128 v[142:145], v2 offset:2048
	ds_read_b128 v[146:149], v2 offset:3072
	v_add_u32_e32 v2, s73, v219
	ds_read_b128 v[150:153], v2
	ds_read_b128 v[154:157], v2 offset:1024
	ds_read_b128 v[158:161], v2 offset:2048
	ds_read_b128 v[162:165], v2 offset:3072
	v_lshl_add_u64 v[4:5], v[226:227], 0, s[36:37]
	v_cndmask_b32_e64 v233, v5, v215, s[10:11]
	v_cndmask_b32_e64 v232, v4, v248, s[10:11]
	v_lshl_add_u64 v[4:5], v[230:231], 0, s[36:37]
	s_add_i32 m0, s58, 0xc000
	ds_read_b128 v[166:169], v249
	ds_read_b128 v[170:173], v249 offset:1024
	ds_read_b128 v[174:177], v249 offset:2048
	ds_read_b128 v[178:181], v249 offset:3072
	ds_read_b128 v[182:185], v249 offset:4096
	ds_read_b128 v[186:189], v249 offset:5120
	ds_read_b128 v[190:193], v249 offset:6144
	ds_read_b128 v[194:197], v249 offset:7168
	global_load_lds_dwordx4 v[4:5], off
	v_lshl_add_u64 v[4:5], v[228:229], 0, s[36:37]
	s_add_i32 m0, s58, 0xe000
	s_nop 0
	global_load_lds_dwordx4 v[4:5], off
	s_waitcnt vmcnt(8)
	s_waitcnt lgkmcnt(0)
	s_barrier
	v_mfma_f32_16x16x32_bf16 v[130:133], v[134:137], v[166:169], v[130:133]
	v_mfma_f32_16x16x32_bf16 v[102:105], v[142:145], v[166:169], v[102:105]
	v_mfma_f32_16x16x32_bf16 v[82:85], v[134:137], v[174:177], v[82:85]
	v_mfma_f32_16x16x32_bf16 v[78:81], v[142:145], v[174:177], v[78:81]
	v_mfma_f32_16x16x32_bf16 v[54:57], v[134:137], v[182:185], v[54:57]
	v_mfma_f32_16x16x32_bf16 v[50:53], v[142:145], v[182:185], v[50:53]
	v_mfma_f32_16x16x32_bf16 v[22:25], v[134:137], v[190:193], v[22:25]
	v_mfma_f32_16x16x32_bf16 v[18:21], v[142:145], v[190:193], v[18:21]
	v_mfma_f32_16x16x32_bf16 v[130:133], v[138:141], v[170:173], v[130:133]
	v_mfma_f32_16x16x32_bf16 v[102:105], v[146:149], v[170:173], v[102:105]
	v_mfma_f32_16x16x32_bf16 v[82:85], v[138:141], v[178:181], v[82:85]
	v_mfma_f32_16x16x32_bf16 v[78:81], v[146:149], v[178:181], v[78:81]
	v_mfma_f32_16x16x32_bf16 v[54:57], v[138:141], v[186:189], v[54:57]
	v_mfma_f32_16x16x32_bf16 v[50:53], v[146:149], v[186:189], v[50:53]
	v_mfma_f32_16x16x32_bf16 v[22:25], v[138:141], v[194:197], v[22:25]
	v_mfma_f32_16x16x32_bf16 v[18:21], v[146:149], v[194:197], v[18:21]
	v_mfma_f32_16x16x32_bf16 v[122:125], v[150:153], v[166:169], v[122:125]
	v_mfma_f32_16x16x32_bf16 v[126:129], v[158:161], v[166:169], v[126:129]
	v_mfma_f32_16x16x32_bf16 v[106:109], v[150:153], v[174:177], v[106:109]
	v_mfma_f32_16x16x32_bf16 v[110:113], v[158:161], v[174:177], v[110:113]
	v_mfma_f32_16x16x32_bf16 v[86:89], v[150:153], v[182:185], v[86:89]
	v_mfma_f32_16x16x32_bf16 v[90:93], v[158:161], v[182:185], v[90:93]
	v_mfma_f32_16x16x32_bf16 v[58:61], v[150:153], v[190:193], v[58:61]
	v_mfma_f32_16x16x32_bf16 v[62:65], v[158:161], v[190:193], v[62:65]
	v_mfma_f32_16x16x32_bf16 v[122:125], v[154:157], v[170:173], v[122:125]
	v_mfma_f32_16x16x32_bf16 v[126:129], v[162:165], v[170:173], v[126:129]
	v_mfma_f32_16x16x32_bf16 v[106:109], v[154:157], v[178:181], v[106:109]
	v_mfma_f32_16x16x32_bf16 v[110:113], v[162:165], v[178:181], v[110:113]
	v_mfma_f32_16x16x32_bf16 v[86:89], v[154:157], v[186:189], v[86:89]
	v_mfma_f32_16x16x32_bf16 v[90:93], v[162:165], v[186:189], v[90:93]
	v_mfma_f32_16x16x32_bf16 v[58:61], v[154:157], v[194:197], v[58:61]
	v_mfma_f32_16x16x32_bf16 v[62:65], v[162:165], v[194:197], v[62:65]
	s_barrier
; #define PG8_STAGE_A(bufoff, base_, nx_, kb_, h_) do { if (GATHER) { if (nx_) PG8_STAGE_G(bufoff, kb_, goN, h_); else PG8_STAGE_G(bufoff, kb_, goC, h_); } \
;         else PG8_STAGE(bufoff, (base_) + (kb_) + (h_) * hstep, voffA); } while (0)
; #define PG8_STAGE(bufoff, gbase, voff) do { _Pragma("unroll") for (int _i = 0; _i < 2; ++_i) \
;         __builtin_amdgcn_global_load_lds((const unsigned*)((const char*)(gbase) + (voff)[_i]), (LAS unsigned*)(lds + (bufoff) + ldsw + _i * 8192), 16, 0, 0); } while (0)
; #define PG8_LDA(dst, b, h) do { _Pragma("unroll") for (int m = 0; m < 4; ++m) _Pragma("unroll") for (int k = 0; k < 2; ++k) dst[m][k] = *(const LAS bf16x8*)(lds + PG8_SA(b, h) + aoff + m * 2048 + k * 1024); } while (0)
; #define PG8_LDB(dst, b, h) do { _Pragma("unroll") for (int n = 0; n < 2; ++n) _Pragma("unroll") for (int k = 0; k < 2; ++k) dst[n][k] = *(const LAS bf16x8*)(lds + PG8_SB(b, h) + boff + n * 2048 + k * 1024); } while (0)
; #define PG8_MMA(ai, bj, At, Bt) do { __builtin_amdgcn_s_setprio(1); _Pragma("unroll") for (int m = 0; m < 4; ++m) _Pragma("unroll") for (int n = 0; n < 2; ++n) _Pragma("unroll") for (int k = 0; k < 2; ++k) \
;         acc[ai][bj][m][n] = __builtin_amdgcn_mfma_f32_16x16x32_bf16(Bt[n][k], At[m][k], acc[ai][bj][m][n], 0, 0, 0); __builtin_amdgcn_s_setprio(0); } while (0)
; #define PG8_WAIT_V(n) asm volatile("s_waitcnt vmcnt(" #n ")" ::: "memory")
; #define PG8_WAIT_L(n) asm volatile("s_waitcnt lgkmcnt(" #n ")" ::: "memory")
; #define PG8_BAR __builtin_amdgcn_s_barrier()
; #define PG8_SCHED __builtin_amdgcn_sched_barrier(0)
; template <class Epi, class Sched, bool GATHER = false>
; __device__ __forceinline__ void gemm_phase(LAS unsigned char* lds, const Gemm g, const Sched& S, const Epi& E, const int tid) {
;     ...
;             PG8_LDA(At, 0, 1); PG8_STAGE(PG8_SB(0, 0), b2, voffB); PG8_STAGE(PG8_SB(0, 1), b2 + hstep, voffB); PG8_STAGE_A(PG8_SA(0, 0), (last ? nA : cA), last, kb2, 0);
;             PG8_WAIT_V(8); PG8_WAIT_L(0); PG8_BAR; PG8_MMA(1, 0, At, B0); PG8_MMA(1, 1, At, B1); PG8_BAR; PG8_SCHED;
;             PG8_LDB(B0, 1, 0); PG8_LDB(B1, 1, 1); PG8_SCHED; PG8_LDA(At, 1, 0); PG8_STAGE_A(PG8_SA(0, 1), (last ? nA : cA), last, kb2, 1);
	s_add_i32 s36, s72, s57
	v_lshl_add_u64 v[234:235], v[232:233], 0, v[202:203]
	s_mov_b32 m0, s36
	ds_read_b128 v[166:169], v249 offset:16384
	ds_read_b128 v[170:173], v249 offset:17408
	ds_read_b128 v[174:177], v249 offset:18432
	ds_read_b128 v[178:181], v249 offset:19456
	ds_read_b128 v[182:185], v249 offset:20480
	ds_read_b128 v[186:189], v249 offset:21504
	ds_read_b128 v[190:193], v249 offset:22528
	ds_read_b128 v[194:197], v249 offset:23552
	global_load_lds_dwordx4 v[234:235], off
	s_add_i32 m0, s36, 0x2000
	s_mov_b64 s[36:37], 0x80000
	v_lshl_add_u64 v[236:237], v[232:233], 0, v[204:205]
	v_lshl_add_u64 v[4:5], v[232:233], 0, s[36:37]
	s_add_i32 s36, s73, s57
	global_load_lds_dwordx4 v[236:237], off
	v_lshl_add_u64 v[238:239], v[4:5], 0, v[202:203]
	s_mov_b32 m0, s36
	v_lshl_add_u64 v[4:5], v[4:5], 0, v[204:205]
	global_load_lds_dwordx4 v[238:239], off
	s_add_i32 m0, s36, 0x2000
	s_add_u32 s36, s12, s71
	s_addc_u32 s37, s13, 0
	v_cndmask_b32_e64 v2, v224, v206, s[10:11]
	global_load_lds_dwordx4 v[4:5], off
	v_lshl_add_u64 v[238:239], s[36:37], 0, v[2:3]
	s_mov_b32 m0, s58
	v_cndmask_b32_e64 v4, v218, v213, s[10:11]
	global_load_lds_dwordx4 v[238:239], off
	s_mov_b32 m0, s59
	s_nop 0
	global_load_lds_dwordx4 v4, s[36:37]
	s_waitcnt vmcnt(8)
	s_waitcnt lgkmcnt(0)
	s_barrier
	v_mfma_f32_16x16x32_bf16 v[42:45], v[134:137], v[166:169], v[42:45]
	v_mfma_f32_16x16x32_bf16 v[26:29], v[142:145], v[166:169], v[26:29]
	v_mfma_f32_16x16x32_bf16 v[14:17], v[134:137], v[174:177], v[14:17]
	v_mfma_f32_16x16x32_bf16 v[66:69], v[142:145], v[174:177], v[66:69]
	v_mfma_f32_16x16x32_bf16 v[46:49], v[134:137], v[182:185], v[46:49]
	v_mfma_f32_16x16x32_bf16 v[30:33], v[142:145], v[182:185], v[30:33]
	v_mfma_f32_16x16x32_bf16 v[10:13], v[134:137], v[190:193], v[10:13]
	v_mfma_f32_16x16x32_bf16 v[4:7], v[142:145], v[190:193], v[6:9]
	v_mfma_f32_16x16x32_bf16 v[42:45], v[138:141], v[170:173], v[42:45]
	v_mfma_f32_16x16x32_bf16 v[26:29], v[146:149], v[170:173], v[26:29]
	v_mfma_f32_16x16x32_bf16 v[14:17], v[138:141], v[178:181], v[14:17]
	v_mfma_f32_16x16x32_bf16 v[66:69], v[146:149], v[178:181], v[66:69]
	v_mfma_f32_16x16x32_bf16 v[46:49], v[138:141], v[186:189], v[46:49]
	v_mfma_f32_16x16x32_bf16 v[30:33], v[146:149], v[186:189], v[30:33]
	v_mfma_f32_16x16x32_bf16 v[10:13], v[138:141], v[194:197], v[10:13]
	v_mfma_f32_16x16x32_bf16 v[4:7], v[146:149], v[194:197], v[4:7]
	v_mfma_f32_16x16x32_bf16 v[118:121], v[150:153], v[166:169], v[118:121]
	v_mfma_f32_16x16x32_bf16 v[114:117], v[158:161], v[166:169], v[114:117]
	v_mfma_f32_16x16x32_bf16 v[98:101], v[150:153], v[174:177], v[98:101]
	v_mfma_f32_16x16x32_bf16 v[94:97], v[158:161], v[174:177], v[94:97]
	v_mfma_f32_16x16x32_bf16 v[74:77], v[150:153], v[182:185], v[74:77]
	v_mfma_f32_16x16x32_bf16 v[70:73], v[158:161], v[182:185], v[70:73]
	v_mfma_f32_16x16x32_bf16 v[38:41], v[150:153], v[190:193], v[38:41]
	v_mfma_f32_16x16x32_bf16 v[34:37], v[158:161], v[190:193], v[34:37]
	v_mfma_f32_16x16x32_bf16 v[118:121], v[154:157], v[170:173], v[118:121]
	v_mfma_f32_16x16x32_bf16 v[114:117], v[162:165], v[170:173], v[114:117]
	v_mfma_f32_16x16x32_bf16 v[98:101], v[154:157], v[178:181], v[98:101]
	v_mfma_f32_16x16x32_bf16 v[94:97], v[162:165], v[178:181], v[94:97]
	v_mfma_f32_16x16x32_bf16 v[74:77], v[154:157], v[186:189], v[74:77]
	v_mfma_f32_16x16x32_bf16 v[70:73], v[162:165], v[186:189], v[70:73]
	v_mfma_f32_16x16x32_bf16 v[38:41], v[154:157], v[194:197], v[38:41]
	v_mfma_f32_16x16x32_bf16 v[34:37], v[162:165], v[194:197], v[34:37]
	s_barrier
	v_add_u32_e32 v2, 0, v219
	v_add_u32_e32 v8, 0x18000, v2
	v_add_u32_e32 v2, 0x1c000, v2
	ds_read_b128 v[150:153], v8
	ds_read_b128 v[154:157], v8 offset:1024
	ds_read_b128 v[158:161], v8 offset:2048
	ds_read_b128 v[162:165], v8 offset:3072
	ds_read_b128 v[134:137], v2
	ds_read_b128 v[138:141], v2 offset:1024
	ds_read_b128 v[142:145], v2 offset:2048
	ds_read_b128 v[146:149], v2 offset:3072
	ds_read_b128 v[190:193], v249 offset:32768
	ds_read_b128 v[194:197], v249 offset:33792
	ds_read_b128 v[182:185], v249 offset:34816
	ds_read_b128 v[186:189], v249 offset:35840
	ds_read_b128 v[174:177], v249 offset:36864
	ds_read_b128 v[178:181], v249 offset:37888
	ds_read_b128 v[166:169], v249 offset:38912
	ds_read_b128 v[170:173], v249 offset:39936
	s_andn2_b64 vcc, exec, s[34:35]
	s_cbranch_vccnz .LBB0_1399
	s_mov_b32 m0, s60
	v_lshl_add_u64 v[8:9], s[36:37], 0, v[220:221]
	global_load_lds_dwordx4 v[8:9], off
	v_mov_b64_e32 v[8:9], v[222:223]
	s_mov_b64 s[72:73], 0xb0000
	v_mov_b32_e32 v2, v218
	s_cbranch_execz .LBB0_1400
	s_branch .LBB0_1401

; #define PG8_STAGE_A(bufoff, base_, nx_, kb_, h_) do { if (GATHER) { if (nx_) PG8_STAGE_G(bufoff, kb_, goN, h_); else PG8_STAGE_G(bufoff, kb_, goC, h_); } \
;         else PG8_STAGE(bufoff, (base_) + (kb_) + (h_) * hstep, voffA); } while (0)
; #define PG8_STAGE(bufoff, gbase, voff) do { _Pragma("unroll") for (int _i = 0; _i < 2; ++_i) \
;         __builtin_amdgcn_global_load_lds((const unsigned*)((const char*)(gbase) + (voff)[_i]), (LAS unsigned*)(lds + (bufoff) + ldsw + _i * 8192), 16, 0, 0); } while (0)
; #define PG8_LDA(dst, b, h) do { _Pragma("unroll") for (int m = 0; m < 4; ++m) _Pragma("unroll") for (int k = 0; k < 2; ++k) dst[m][k] = *(const LAS bf16x8*)(lds + PG8_SA(b, h) + aoff + m * 2048 + k * 1024); } while (0)
; #define PG8_LDB(dst, b, h) do { _Pragma("unroll") for (int n = 0; n < 2; ++n) _Pragma("unroll") for (int k = 0; k < 2; ++k) dst[n][k] = *(const LAS bf16x8*)(lds + PG8_SB(b, h) + boff + n * 2048 + k * 1024); } while (0)
; #define PG8_MMA(ai, bj, At, Bt) do { __builtin_amdgcn_s_setprio(1); _Pragma("unroll") for (int m = 0; m < 4; ++m) _Pragma("unroll") for (int n = 0; n < 2; ++n) _Pragma("unroll") for (int k = 0; k < 2; ++k) \
;         acc[ai][bj][m][n] = __builtin_amdgcn_mfma_f32_16x16x32_bf16(Bt[n][k], At[m][k], acc[ai][bj][m][n], 0, 0, 0); __builtin_amdgcn_s_setprio(0); } while (0)
; #define PG8_WAIT_V(n) asm volatile("s_waitcnt vmcnt(" #n ")" ::: "memory")
; #define PG8_WAIT_L(n) asm volatile("s_waitcnt lgkmcnt(" #n ")" ::: "memory")
; #define PG8_BAR __builtin_amdgcn_s_barrier()
; #define PG8_SCHED __builtin_amdgcn_sched_barrier(0)
; template <class Epi, class Sched, bool GATHER = false>
; __device__ __forceinline__ void gemm_phase(LAS unsigned char* lds, const Gemm g, const Sched& S, const Epi& E, const int tid) {
;     ...
;             PG8_LDB(B0, 1, 0); PG8_LDB(B1, 1, 1); PG8_SCHED; PG8_LDA(At, 1, 0); PG8_STAGE_A(PG8_SA(0, 1), (last ? nA : cA), last, kb2, 1);
;             PG8_WAIT_V(8); PG8_WAIT_L(0); PG8_BAR; PG8_MMA(0, 0, At, B0); PG8_MMA(0, 1, At, B1); PG8_BAR; PG8_SCHED;
;             PG8_LDA(At, 1, 1); PG8_STAGE(PG8_SB(1, 0), b3, voffB); PG8_STAGE(PG8_SB(1, 1), b3 + hstep, voffB); PG8_STAGE_A(PG8_SA(1, 0), (last ? nA : cA), last, kb3, 0);
;             PG8_WAIT_V(8); PG8_WAIT_L(0); PG8_BAR; PG8_MMA(1, 0, At, B0); PG8_MMA(1, 1, At, B1); PG8_BAR; PG8_SCHED;
;     ...
;         }
.LBB0_1401:
	v_lshl_add_u64 v[8:9], s[36:37], 0, v[8:9]
	s_mov_b32 m0, s61
	s_nop 0
	global_load_lds_dwordx4 v[8:9], off
	s_waitcnt vmcnt(8)
	s_waitcnt lgkmcnt(0)
	s_barrier
	v_mfma_f32_16x16x32_bf16 v[130:133], v[150:153], v[190:193], v[130:133]
	v_mfma_f32_16x16x32_bf16 v[102:105], v[158:161], v[190:193], v[102:105]
	v_mfma_f32_16x16x32_bf16 v[82:85], v[150:153], v[182:185], v[82:85]
	v_mfma_f32_16x16x32_bf16 v[78:81], v[158:161], v[182:185], v[78:81]
	v_mfma_f32_16x16x32_bf16 v[54:57], v[150:153], v[174:177], v[54:57]
	v_mfma_f32_16x16x32_bf16 v[50:53], v[158:161], v[174:177], v[50:53]
	v_mfma_f32_16x16x32_bf16 v[22:25], v[150:153], v[166:169], v[22:25]
	v_mfma_f32_16x16x32_bf16 v[18:21], v[158:161], v[166:169], v[18:21]
	v_mfma_f32_16x16x32_bf16 v[130:133], v[154:157], v[194:197], v[130:133]
	v_mfma_f32_16x16x32_bf16 v[102:105], v[162:165], v[194:197], v[102:105]
	v_mfma_f32_16x16x32_bf16 v[82:85], v[154:157], v[186:189], v[82:85]
	v_mfma_f32_16x16x32_bf16 v[78:81], v[162:165], v[186:189], v[78:81]
	v_mfma_f32_16x16x32_bf16 v[54:57], v[154:157], v[178:181], v[54:57]
	v_mfma_f32_16x16x32_bf16 v[50:53], v[162:165], v[178:181], v[50:53]
	v_mfma_f32_16x16x32_bf16 v[22:25], v[154:157], v[170:173], v[22:25]
	v_mfma_f32_16x16x32_bf16 v[18:21], v[162:165], v[170:173], v[18:21]
	v_mfma_f32_16x16x32_bf16 v[122:125], v[134:137], v[190:193], v[122:125]
	v_mfma_f32_16x16x32_bf16 v[126:129], v[142:145], v[190:193], v[126:129]
	v_mfma_f32_16x16x32_bf16 v[106:109], v[134:137], v[182:185], v[106:109]
	v_mfma_f32_16x16x32_bf16 v[110:113], v[142:145], v[182:185], v[110:113]
	v_mfma_f32_16x16x32_bf16 v[86:89], v[134:137], v[174:177], v[86:89]
	v_mfma_f32_16x16x32_bf16 v[90:93], v[142:145], v[174:177], v[90:93]
	v_mfma_f32_16x16x32_bf16 v[58:61], v[134:137], v[166:169], v[58:61]
	v_mfma_f32_16x16x32_bf16 v[62:65], v[142:145], v[166:169], v[62:65]
	v_mfma_f32_16x16x32_bf16 v[122:125], v[138:141], v[194:197], v[122:125]
	v_mfma_f32_16x16x32_bf16 v[126:129], v[146:149], v[194:197], v[126:129]
	v_mfma_f32_16x16x32_bf16 v[106:109], v[138:141], v[186:189], v[106:109]
	v_mfma_f32_16x16x32_bf16 v[110:113], v[146:149], v[186:189], v[110:113]
	v_mfma_f32_16x16x32_bf16 v[86:89], v[138:141], v[178:181], v[86:89]
	v_mfma_f32_16x16x32_bf16 v[90:93], v[146:149], v[178:181], v[90:93]
	v_mfma_f32_16x16x32_bf16 v[58:61], v[138:141], v[170:173], v[58:61]
	v_mfma_f32_16x16x32_bf16 v[62:65], v[146:149], v[170:173], v[62:65]
	s_barrier
	s_mov_b32 m0, s62
	v_lshl_add_u64 v[8:9], v[234:235], 0, s[0:1]
	ds_read_b128 v[166:169], v249 offset:49152
	ds_read_b128 v[170:173], v249 offset:50176
	ds_read_b128 v[174:177], v249 offset:51200
	ds_read_b128 v[178:181], v249 offset:52224
	ds_read_b128 v[182:185], v249 offset:53248
	ds_read_b128 v[186:189], v249 offset:54272
	ds_read_b128 v[190:193], v249 offset:55296
	ds_read_b128 v[194:197], v249 offset:56320
	global_load_lds_dwordx4 v[8:9], off
	v_lshl_add_u64 v[8:9], v[236:237], 0, s[0:1]
	s_mov_b32 m0, s33
	s_mov_b64 s[10:11], 0x80080
	global_load_lds_dwordx4 v[8:9], off
	v_lshl_add_u64 v[8:9], v[232:233], 0, s[10:11]
	v_lshl_add_u64 v[232:233], v[8:9], 0, v[202:203]
	s_mov_b32 m0, s63
	v_lshl_add_u64 v[8:9], v[8:9], 0, v[204:205]
	global_load_lds_dwordx4 v[232:233], off
	s_mov_b32 m0, s64
	s_nop 0
	global_load_lds_dwordx4 v[8:9], off
	v_lshl_add_u64 v[8:9], v[238:239], 0, s[0:1]
	s_mov_b32 m0, s48
	s_nop 0
	global_load_lds_dwordx4 v[8:9], off
	v_lshl_add_u64 v[8:9], s[36:37], 0, v[2:3]
	v_lshl_add_u64 v[8:9], v[8:9], 0, s[0:1]
	s_mov_b32 m0, s49
	s_nop 0
	global_load_lds_dwordx4 v[8:9], off
	s_waitcnt vmcnt(8)
	s_waitcnt lgkmcnt(0)
	s_barrier
	v_mfma_f32_16x16x32_bf16 v[42:45], v[150:153], v[166:169], v[42:45]
	v_mfma_f32_16x16x32_bf16 v[26:29], v[158:161], v[166:169], v[26:29]
	v_mfma_f32_16x16x32_bf16 v[14:17], v[150:153], v[174:177], v[14:17]
	v_mfma_f32_16x16x32_bf16 v[66:69], v[158:161], v[174:177], v[66:69]
	v_mfma_f32_16x16x32_bf16 v[46:49], v[150:153], v[182:185], v[46:49]
	v_mfma_f32_16x16x32_bf16 v[30:33], v[158:161], v[182:185], v[30:33]
	v_mfma_f32_16x16x32_bf16 v[8:11], v[150:153], v[190:193], v[10:13]
	v_mfma_f32_16x16x32_bf16 v[4:7], v[158:161], v[190:193], v[4:7]
	v_mfma_f32_16x16x32_bf16 v[42:45], v[154:157], v[170:173], v[42:45]
	v_mfma_f32_16x16x32_bf16 v[26:29], v[162:165], v[170:173], v[26:29]
	v_mfma_f32_16x16x32_bf16 v[14:17], v[154:157], v[178:181], v[14:17]
	v_mfma_f32_16x16x32_bf16 v[66:69], v[162:165], v[178:181], v[66:69]
	v_mfma_f32_16x16x32_bf16 v[46:49], v[154:157], v[186:189], v[46:49]
	v_mfma_f32_16x16x32_bf16 v[30:33], v[162:165], v[186:189], v[30:33]
	v_mfma_f32_16x16x32_bf16 v[10:13], v[154:157], v[194:197], v[8:11]
	v_mfma_f32_16x16x32_bf16 v[6:9], v[162:165], v[194:197], v[4:7]
	v_mfma_f32_16x16x32_bf16 v[118:121], v[134:137], v[166:169], v[118:121]
	v_mfma_f32_16x16x32_bf16 v[114:117], v[142:145], v[166:169], v[114:117]
	v_mfma_f32_16x16x32_bf16 v[98:101], v[134:137], v[174:177], v[98:101]
	v_mfma_f32_16x16x32_bf16 v[94:97], v[142:145], v[174:177], v[94:97]
	v_mfma_f32_16x16x32_bf16 v[74:77], v[134:137], v[182:185], v[74:77]
	v_mfma_f32_16x16x32_bf16 v[70:73], v[142:145], v[182:185], v[70:73]
	v_mfma_f32_16x16x32_bf16 v[38:41], v[134:137], v[190:193], v[38:41]
	v_mfma_f32_16x16x32_bf16 v[34:37], v[142:145], v[190:193], v[34:37]
	v_mfma_f32_16x16x32_bf16 v[118:121], v[138:141], v[170:173], v[118:121]
	v_mfma_f32_16x16x32_bf16 v[114:117], v[146:149], v[170:173], v[114:117]
	v_mfma_f32_16x16x32_bf16 v[98:101], v[138:141], v[178:181], v[98:101]
	v_mfma_f32_16x16x32_bf16 v[94:97], v[146:149], v[178:181], v[94:97]
	v_mfma_f32_16x16x32_bf16 v[74:77], v[138:141], v[186:189], v[74:77]
	v_mfma_f32_16x16x32_bf16 v[70:73], v[146:149], v[186:189], v[70:73]
	v_mfma_f32_16x16x32_bf16 v[38:41], v[138:141], v[194:197], v[38:41]
	v_mfma_f32_16x16x32_bf16 v[34:37], v[146:149], v[194:197], v[34:37]
	s_barrier
	s_add_i32 s70, s70, 2
	s_cmp_gt_u32 s70, 29
	s_cbranch_scc1 .LBB0_1403
	s_mov_b64 s[36:37], s[30:31]
	s_branch .LBB0_1395

; #define PG8_STAGE_A(bufoff, base_, nx_, kb_, h_) do { if (GATHER) { if (nx_) PG8_STAGE_G(bufoff, kb_, goN, h_); else PG8_STAGE_G(bufoff, kb_, goC, h_); } \
;         else PG8_STAGE(bufoff, (base_) + (kb_) + (h_) * hstep, voffA); } while (0)
; #define PG8_STAGE(bufoff, gbase, voff) do { _Pragma("unroll") for (int _i = 0; _i < 2; ++_i) \
;         __builtin_amdgcn_global_load_lds((const unsigned*)((const char*)(gbase) + (voff)[_i]), (LAS unsigned*)(lds + (bufoff) + ldsw + _i * 8192), 16, 0, 0); } while (0)
; #define PG8_LDA(dst, b, h) do { _Pragma("unroll") for (int m = 0; m < 4; ++m) _Pragma("unroll") for (int k = 0; k < 2; ++k) dst[m][k] = *(const LAS bf16x8*)(lds + PG8_SA(b, h) + aoff + m * 2048 + k * 1024); } while (0)
; #define PG8_LDB(dst, b, h) do { _Pragma("unroll") for (int n = 0; n < 2; ++n) _Pragma("unroll") for (int k = 0; k < 2; ++k) dst[n][k] = *(const LAS bf16x8*)(lds + PG8_SB(b, h) + boff + n * 2048 + k * 1024); } while (0)
; #define PG8_MMA(ai, bj, At, Bt) do { __builtin_amdgcn_s_setprio(1); _Pragma("unroll") for (int m = 0; m < 4; ++m) _Pragma("unroll") for (int n = 0; n < 2; ++n) _Pragma("unroll") for (int k = 0; k < 2; ++k) \
;         acc[ai][bj][m][n] = __builtin_amdgcn_mfma_f32_16x16x32_bf16(Bt[n][k], At[m][k], acc[ai][bj][m][n], 0, 0, 0); __builtin_amdgcn_s_setprio(0); } while (0)
; #define PG8_WAIT_V(n) asm volatile("s_waitcnt vmcnt(" #n ")" ::: "memory")
; #define PG8_WAIT_L(n) asm volatile("s_waitcnt lgkmcnt(" #n ")" ::: "memory")
; #define PG8_BAR __builtin_amdgcn_s_barrier()
; #define PG8_SCHED __builtin_amdgcn_sched_barrier(0)
; template <class Epi, class Sched, bool GATHER = false>
; __device__ __forceinline__ void gemm_phase(LAS unsigned char* lds, const Gemm g, const Sched& S, const Epi& E, const int tid) {
;     ...
;             PG8_LDB(B0, 0, 0); PG8_LDB(B1, 0, 1); PG8_SCHED; PG8_LDA(At, 0, 0); PG8_STAGE_A(PG8_SA(1, 1), cA, false, kb1, 1);
;             PG8_WAIT_V(8); PG8_WAIT_L(0); PG8_BAR; PG8_MMA(0, 0, At, B0); PG8_MMA(0, 1, At, B1); PG8_BAR; PG8_SCHED;
;             PG8_LDA(At, 0, 1); PG8_STAGE(PG8_SB(0, 0), b2, voffB); PG8_STAGE(PG8_SB(0, 1), b2 + hstep, voffB); PG8_STAGE_A(PG8_SA(0, 0), (last ? nA : cA), last, kb2, 0);
;             PG8_WAIT_V(8); PG8_WAIT_L(0); PG8_BAR; PG8_MMA(1, 0, At, B0); PG8_MMA(1, 1, At, B1); PG8_BAR; PG8_SCHED;
.LBB0_1483:
	s_add_u32 s28, s34, 0x100
	s_addc_u32 s29, s35, 0
	s_add_u32 s30, s56, s34
	s_addc_u32 s31, s57, s35
	s_add_i32 s59, 0, 0x10000
	s_add_i32 s60, 0, 0x14000
	v_add_u32_e32 v2, s59, v149
	ds_read_b128 v[152:155], v2
	ds_read_b128 v[156:159], v2 offset:1024
	ds_read_b128 v[160:163], v2 offset:2048
	ds_read_b128 v[164:167], v2 offset:3072
	v_add_u32_e32 v2, s60, v149
	ds_read_b128 v[168:171], v2
	ds_read_b128 v[172:175], v2 offset:1024
	ds_read_b128 v[176:179], v2 offset:2048
	ds_read_b128 v[180:183], v2 offset:3072
	s_add_i32 s62, s59, s33
	s_add_i32 m0, s44, 0xc000
	s_add_i32 s61, s44, 0xe000
	s_add_i32 s59, s62, 0x2000
	s_cmpk_eq_i32 s58, 0x54
	s_cselect_b32 s31, s25, s31
	s_cselect_b32 s30, s24, s30
	v_lshl_add_u64 v[218:219], v[4:5], 0, s[34:35]
	ds_read_b128 v[184:187], v151
	ds_read_b128 v[188:191], v151 offset:1024
	ds_read_b128 v[192:195], v151 offset:2048
	ds_read_b128 v[196:199], v151 offset:3072
	ds_read_b128 v[202:205], v151 offset:4096
	ds_read_b128 v[206:209], v151 offset:5120
	ds_read_b128 v[210:213], v151 offset:6144
	ds_read_b128 v[214:217], v151 offset:7168
	global_load_lds_dwordx4 v[218:219], off
	v_lshl_add_u64 v[218:219], v[146:147], 0, s[34:35]
	s_mov_b32 m0, s61
	s_nop 0
	global_load_lds_dwordx4 v[218:219], off
	s_waitcnt vmcnt(8)
	s_waitcnt lgkmcnt(0)
	s_barrier
	v_mfma_f32_16x16x32_bf16 v[86:89], v[152:155], v[184:187], v[86:89]
	v_mfma_f32_16x16x32_bf16 v[18:21], v[160:163], v[184:187], v[18:21]
	v_mfma_f32_16x16x32_bf16 v[6:9], v[152:155], v[192:195], v[6:9]
	v_mfma_f32_16x16x32_bf16 v[22:25], v[160:163], v[192:195], v[22:25]
	v_mfma_f32_16x16x32_bf16 v[10:13], v[152:155], v[202:205], v[10:13]
	v_mfma_f32_16x16x32_bf16 v[26:29], v[160:163], v[202:205], v[26:29]
	v_mfma_f32_16x16x32_bf16 v[14:17], v[152:155], v[210:213], v[14:17]
	v_mfma_f32_16x16x32_bf16 v[30:33], v[160:163], v[210:213], v[30:33]
	v_mfma_f32_16x16x32_bf16 v[86:89], v[156:159], v[188:191], v[86:89]
	v_mfma_f32_16x16x32_bf16 v[18:21], v[164:167], v[188:191], v[18:21]
	v_mfma_f32_16x16x32_bf16 v[6:9], v[156:159], v[196:199], v[6:9]
	v_mfma_f32_16x16x32_bf16 v[22:25], v[164:167], v[196:199], v[22:25]
	v_mfma_f32_16x16x32_bf16 v[10:13], v[156:159], v[206:209], v[10:13]
	v_mfma_f32_16x16x32_bf16 v[26:29], v[164:167], v[206:209], v[26:29]
	v_mfma_f32_16x16x32_bf16 v[14:17], v[156:159], v[214:217], v[14:17]
	v_mfma_f32_16x16x32_bf16 v[30:33], v[164:167], v[214:217], v[30:33]
	v_mfma_f32_16x16x32_bf16 v[34:37], v[168:171], v[184:187], v[34:37]
	v_mfma_f32_16x16x32_bf16 v[50:53], v[176:179], v[184:187], v[50:53]
	v_mfma_f32_16x16x32_bf16 v[38:41], v[168:171], v[192:195], v[38:41]
	v_mfma_f32_16x16x32_bf16 v[54:57], v[176:179], v[192:195], v[54:57]
	v_mfma_f32_16x16x32_bf16 v[42:45], v[168:171], v[202:205], v[42:45]
	v_mfma_f32_16x16x32_bf16 v[62:65], v[176:179], v[202:205], v[62:65]
	v_mfma_f32_16x16x32_bf16 v[46:49], v[168:171], v[210:213], v[46:49]
	v_mfma_f32_16x16x32_bf16 v[70:73], v[176:179], v[210:213], v[70:73]
	v_mfma_f32_16x16x32_bf16 v[34:37], v[172:175], v[188:191], v[34:37]
	v_mfma_f32_16x16x32_bf16 v[50:53], v[180:183], v[188:191], v[50:53]
	v_mfma_f32_16x16x32_bf16 v[38:41], v[172:175], v[196:199], v[38:41]
	v_mfma_f32_16x16x32_bf16 v[54:57], v[180:183], v[196:199], v[54:57]
	v_mfma_f32_16x16x32_bf16 v[42:45], v[172:175], v[206:209], v[42:45]
	v_mfma_f32_16x16x32_bf16 v[62:65], v[180:183], v[206:209], v[62:65]
	v_mfma_f32_16x16x32_bf16 v[46:49], v[172:175], v[214:217], v[46:49]
	v_mfma_f32_16x16x32_bf16 v[70:73], v[180:183], v[214:217], v[70:73]
	s_barrier
	s_mov_b32 m0, s62
	v_lshl_add_u64 v[218:219], s[30:31], 0, v[136:137]
	ds_read_b128 v[184:187], v151 offset:16384
	ds_read_b128 v[188:191], v151 offset:17408
	ds_read_b128 v[192:195], v151 offset:18432
	ds_read_b128 v[196:199], v151 offset:19456
	ds_read_b128 v[202:205], v151 offset:20480
	ds_read_b128 v[206:209], v151 offset:21504
	ds_read_b128 v[210:213], v151 offset:22528
	ds_read_b128 v[214:217], v151 offset:23552
	global_load_lds_dwordx4 v[218:219], off
	s_mov_b32 m0, s59
	s_cselect_b32 s59, 0, s29
	s_cselect_b32 s61, 0, s28
	s_cselect_b32 s62, s11, s15
	s_cselect_b32 s63, s10, s14
	s_add_u32 s34, s30, 0x160000
	v_lshl_add_u64 v[220:221], s[30:31], 0, v[140:141]
	s_addc_u32 s35, s31, 0
	s_add_i32 s60, s60, s33
	global_load_lds_dwordx4 v[220:221], off
	v_lshl_add_u64 v[222:223], s[34:35], 0, v[136:137]
	s_mov_b32 m0, s60
	s_nop 0
	global_load_lds_dwordx4 v[222:223], off
	s_add_i32 m0, s60, 0x2000
	v_lshl_add_u64 v[222:223], s[34:35], 0, v[140:141]
	s_add_u32 s34, s63, s61
	s_addc_u32 s35, s62, s59
	global_load_lds_dwordx4 v[222:223], off
	v_lshl_add_u64 v[222:223], s[34:35], 0, v[134:135]
	s_mov_b32 m0, s44
	v_lshl_add_u64 v[224:225], s[34:35], 0, v[138:139]
	global_load_lds_dwordx4 v[222:223], off
	s_mov_b32 m0, s45
	s_nop 0
	global_load_lds_dwordx4 v[224:225], off
	s_waitcnt vmcnt(8)
	s_waitcnt lgkmcnt(0)
	s_barrier
; #define PG8_STAGE_A(bufoff, base_, nx_, kb_, h_) do { if (GATHER) { if (nx_) PG8_STAGE_G(bufoff, kb_, goN, h_); else PG8_STAGE_G(bufoff, kb_, goC, h_); } \
;         else PG8_STAGE(bufoff, (base_) + (kb_) + (h_) * hstep, voffA); } while (0)
; #define PG8_LDA(dst, b, h) do { _Pragma("unroll") for (int m = 0; m < 4; ++m) _Pragma("unroll") for (int k = 0; k < 2; ++k) dst[m][k] = *(const LAS bf16x8*)(lds + PG8_SA(b, h) + aoff + m * 2048 + k * 1024); } while (0)
; #define PG8_LDB(dst, b, h) do { _Pragma("unroll") for (int n = 0; n < 2; ++n) _Pragma("unroll") for (int k = 0; k < 2; ++k) dst[n][k] = *(const LAS bf16x8*)(lds + PG8_SB(b, h) + boff + n * 2048 + k * 1024); } while (0)
; #define PG8_MMA(ai, bj, At, Bt) do { __builtin_amdgcn_s_setprio(1); _Pragma("unroll") for (int m = 0; m < 4; ++m) _Pragma("unroll") for (int n = 0; n < 2; ++n) _Pragma("unroll") for (int k = 0; k < 2; ++k) \
;         acc[ai][bj][m][n] = __builtin_amdgcn_mfma_f32_16x16x32_bf16(Bt[n][k], At[m][k], acc[ai][bj][m][n], 0, 0, 0); __builtin_amdgcn_s_setprio(0); } while (0)
; #define PG8_WAIT_V(n) asm volatile("s_waitcnt vmcnt(" #n ")" ::: "memory")
; #define PG8_WAIT_L(n) asm volatile("s_waitcnt lgkmcnt(" #n ")" ::: "memory")
; #define PG8_BAR __builtin_amdgcn_s_barrier()
; #define PG8_SCHED __builtin_amdgcn_sched_barrier(0)
; template <class Epi, class Sched, bool GATHER = false>
; __device__ __forceinline__ void gemm_phase(LAS unsigned char* lds, const Gemm g, const Sched& S, const Epi& E, const int tid) {
;     ...
;             PG8_WAIT_V(8); PG8_WAIT_L(0); PG8_BAR; PG8_MMA(1, 0, At, B0); PG8_MMA(1, 1, At, B1); PG8_BAR; PG8_SCHED;
;             PG8_LDB(B0, 1, 0); PG8_LDB(B1, 1, 1); PG8_SCHED; PG8_LDA(At, 1, 0); PG8_STAGE_A(PG8_SA(0, 1), (last ? nA : cA), last, kb2, 1);
;             PG8_WAIT_V(8); PG8_WAIT_L(0); PG8_BAR; PG8_MMA(0, 0, At, B0); PG8_MMA(0, 1, At, B1); PG8_BAR; PG8_SCHED;
	v_mfma_f32_16x16x32_bf16 v[58:61], v[152:155], v[184:187], v[58:61]
	v_mfma_f32_16x16x32_bf16 v[78:81], v[160:163], v[184:187], v[78:81]
	v_mfma_f32_16x16x32_bf16 v[66:69], v[152:155], v[192:195], v[66:69]
	v_mfma_f32_16x16x32_bf16 v[82:85], v[160:163], v[192:195], v[82:85]
	v_mfma_f32_16x16x32_bf16 v[74:77], v[152:155], v[202:205], v[74:77]
	v_mfma_f32_16x16x32_bf16 v[98:101], v[160:163], v[202:205], v[98:101]
	v_mfma_f32_16x16x32_bf16 v[90:93], v[152:155], v[210:213], v[90:93]
	v_mfma_f32_16x16x32_bf16 v[94:97], v[160:163], v[210:213], v[94:97]
	v_mfma_f32_16x16x32_bf16 v[58:61], v[156:159], v[188:191], v[58:61]
	v_mfma_f32_16x16x32_bf16 v[78:81], v[164:167], v[188:191], v[78:81]
	v_mfma_f32_16x16x32_bf16 v[66:69], v[156:159], v[196:199], v[66:69]
	v_mfma_f32_16x16x32_bf16 v[82:85], v[164:167], v[196:199], v[82:85]
	v_mfma_f32_16x16x32_bf16 v[74:77], v[156:159], v[206:209], v[74:77]
	v_mfma_f32_16x16x32_bf16 v[98:101], v[164:167], v[206:209], v[98:101]
	v_mfma_f32_16x16x32_bf16 v[90:93], v[156:159], v[214:217], v[90:93]
	v_mfma_f32_16x16x32_bf16 v[94:97], v[164:167], v[214:217], v[94:97]
	v_mfma_f32_16x16x32_bf16 v[114:117], v[168:171], v[184:187], v[114:117]
	v_mfma_f32_16x16x32_bf16 v[130:133], v[176:179], v[184:187], v[130:133]
	v_mfma_f32_16x16x32_bf16 v[110:113], v[168:171], v[192:195], v[110:113]
	v_mfma_f32_16x16x32_bf16 v[126:129], v[176:179], v[192:195], v[126:129]
	v_mfma_f32_16x16x32_bf16 v[106:109], v[168:171], v[202:205], v[106:109]
	v_mfma_f32_16x16x32_bf16 v[122:125], v[176:179], v[202:205], v[122:125]
	v_mfma_f32_16x16x32_bf16 v[102:105], v[168:171], v[210:213], v[102:105]
	v_mfma_f32_16x16x32_bf16 v[118:121], v[176:179], v[210:213], v[118:121]
	v_mfma_f32_16x16x32_bf16 v[114:117], v[172:175], v[188:191], v[114:117]
	v_mfma_f32_16x16x32_bf16 v[130:133], v[180:183], v[188:191], v[130:133]
	v_mfma_f32_16x16x32_bf16 v[110:113], v[172:175], v[196:199], v[110:113]
	v_mfma_f32_16x16x32_bf16 v[126:129], v[180:183], v[196:199], v[126:129]
	v_mfma_f32_16x16x32_bf16 v[106:109], v[172:175], v[206:209], v[106:109]
	v_mfma_f32_16x16x32_bf16 v[122:125], v[180:183], v[206:209], v[122:125]
	v_mfma_f32_16x16x32_bf16 v[102:105], v[172:175], v[214:217], v[102:105]
	v_mfma_f32_16x16x32_bf16 v[118:121], v[180:183], v[214:217], v[118:121]
	s_barrier
	s_add_i32 s59, 0, 0x18000
	v_add_u32_e32 v2, s59, v149
	s_add_i32 s60, 0, 0x1c000
	ds_read_b128 v[152:155], v2
	ds_read_b128 v[156:159], v2 offset:1024
	ds_read_b128 v[160:163], v2 offset:2048
	ds_read_b128 v[164:167], v2 offset:3072
	v_add_u32_e32 v2, s60, v149
	ds_read_b128 v[168:171], v2
	ds_read_b128 v[172:175], v2 offset:1024
	ds_read_b128 v[176:179], v2 offset:2048
	ds_read_b128 v[180:183], v2 offset:3072
	s_add_u32 s34, s34, 0x160000
	s_addc_u32 s35, s35, 0
	s_mov_b32 m0, s46
	v_lshl_add_u64 v[226:227], s[34:35], 0, v[134:135]
	ds_read_b128 v[184:187], v151 offset:32768
	ds_read_b128 v[188:191], v151 offset:33792
	ds_read_b128 v[192:195], v151 offset:34816
	ds_read_b128 v[196:199], v151 offset:35840
	ds_read_b128 v[202:205], v151 offset:36864
	ds_read_b128 v[206:209], v151 offset:37888
	ds_read_b128 v[210:213], v151 offset:38912
	ds_read_b128 v[214:217], v151 offset:39936
	global_load_lds_dwordx4 v[226:227], off
	v_lshl_add_u64 v[226:227], s[34:35], 0, v[138:139]
	s_mov_b32 m0, s47
	s_nop 0
	global_load_lds_dwordx4 v[226:227], off
	s_waitcnt vmcnt(8)
	s_waitcnt lgkmcnt(0)
	s_barrier
	v_mfma_f32_16x16x32_bf16 v[86:89], v[152:155], v[184:187], v[86:89]
	v_mfma_f32_16x16x32_bf16 v[18:21], v[160:163], v[184:187], v[18:21]
	v_mfma_f32_16x16x32_bf16 v[6:9], v[152:155], v[192:195], v[6:9]
	v_mfma_f32_16x16x32_bf16 v[22:25], v[160:163], v[192:195], v[22:25]
	v_mfma_f32_16x16x32_bf16 v[10:13], v[152:155], v[202:205], v[10:13]
	v_mfma_f32_16x16x32_bf16 v[26:29], v[160:163], v[202:205], v[26:29]
	v_mfma_f32_16x16x32_bf16 v[14:17], v[152:155], v[210:213], v[14:17]
	v_mfma_f32_16x16x32_bf16 v[30:33], v[160:163], v[210:213], v[30:33]
	v_mfma_f32_16x16x32_bf16 v[86:89], v[156:159], v[188:191], v[86:89]
	v_mfma_f32_16x16x32_bf16 v[18:21], v[164:167], v[188:191], v[18:21]
	v_mfma_f32_16x16x32_bf16 v[6:9], v[156:159], v[196:199], v[6:9]
	v_mfma_f32_16x16x32_bf16 v[22:25], v[164:167], v[196:199], v[22:25]
	v_mfma_f32_16x16x32_bf16 v[10:13], v[156:159], v[206:209], v[10:13]
	v_mfma_f32_16x16x32_bf16 v[26:29], v[164:167], v[206:209], v[26:29]
	v_mfma_f32_16x16x32_bf16 v[14:17], v[156:159], v[214:217], v[14:17]
	v_mfma_f32_16x16x32_bf16 v[30:33], v[164:167], v[214:217], v[30:33]
	v_mfma_f32_16x16x32_bf16 v[34:37], v[168:171], v[184:187], v[34:37]
	v_mfma_f32_16x16x32_bf16 v[50:53], v[176:179], v[184:187], v[50:53]
	v_mfma_f32_16x16x32_bf16 v[38:41], v[168:171], v[192:195], v[38:41]
	v_mfma_f32_16x16x32_bf16 v[54:57], v[176:179], v[192:195], v[54:57]
	v_mfma_f32_16x16x32_bf16 v[42:45], v[168:171], v[202:205], v[42:45]
	v_mfma_f32_16x16x32_bf16 v[62:65], v[176:179], v[202:205], v[62:65]
	v_mfma_f32_16x16x32_bf16 v[46:49], v[168:171], v[210:213], v[46:49]
	v_mfma_f32_16x16x32_bf16 v[70:73], v[176:179], v[210:213], v[70:73]
	v_mfma_f32_16x16x32_bf16 v[34:37], v[172:175], v[188:191], v[34:37]
	v_mfma_f32_16x16x32_bf16 v[50:53], v[180:183], v[188:191], v[50:53]
	v_mfma_f32_16x16x32_bf16 v[38:41], v[172:175], v[196:199], v[38:41]
	v_mfma_f32_16x16x32_bf16 v[54:57], v[180:183], v[196:199], v[54:57]
	v_mfma_f32_16x16x32_bf16 v[42:45], v[172:175], v[206:209], v[42:45]
	v_mfma_f32_16x16x32_bf16 v[62:65], v[180:183], v[206:209], v[62:65]
	v_mfma_f32_16x16x32_bf16 v[46:49], v[172:175], v[214:217], v[46:49]
	v_mfma_f32_16x16x32_bf16 v[70:73], v[180:183], v[214:217], v[70:73]
	s_barrier
; #define PG8_STAGE_A(bufoff, base_, nx_, kb_, h_) do { if (GATHER) { if (nx_) PG8_STAGE_G(bufoff, kb_, goN, h_); else PG8_STAGE_G(bufoff, kb_, goC, h_); } \
;         else PG8_STAGE(bufoff, (base_) + (kb_) + (h_) * hstep, voffA); } while (0)
; #define PG8_STAGE(bufoff, gbase, voff) do { _Pragma("unroll") for (int _i = 0; _i < 2; ++_i) \
;         __builtin_amdgcn_global_load_lds((const unsigned*)((const char*)(gbase) + (voff)[_i]), (LAS unsigned*)(lds + (bufoff) + ldsw + _i * 8192), 16, 0, 0); } while (0)
; #define PG8_LDA(dst, b, h) do { _Pragma("unroll") for (int m = 0; m < 4; ++m) _Pragma("unroll") for (int k = 0; k < 2; ++k) dst[m][k] = *(const LAS bf16x8*)(lds + PG8_SA(b, h) + aoff + m * 2048 + k * 1024); } while (0)
; #define PG8_MMA(ai, bj, At, Bt) do { __builtin_amdgcn_s_setprio(1); _Pragma("unroll") for (int m = 0; m < 4; ++m) _Pragma("unroll") for (int n = 0; n < 2; ++n) _Pragma("unroll") for (int k = 0; k < 2; ++k) \
;         acc[ai][bj][m][n] = __builtin_amdgcn_mfma_f32_16x16x32_bf16(Bt[n][k], At[m][k], acc[ai][bj][m][n], 0, 0, 0); __builtin_amdgcn_s_setprio(0); } while (0)
; #define PG8_WAIT_V(n) asm volatile("s_waitcnt vmcnt(" #n ")" ::: "memory")
; #define PG8_WAIT_L(n) asm volatile("s_waitcnt lgkmcnt(" #n ")" ::: "memory")
; #define PG8_BAR __builtin_amdgcn_s_barrier()
; #define PG8_SCHED __builtin_amdgcn_sched_barrier(0)
; template <class Epi, class Sched, bool GATHER = false>
; __device__ __forceinline__ void gemm_phase(LAS unsigned char* lds, const Gemm g, const Sched& S, const Epi& E, const int tid) {
;     ...
;             PG8_LDA(At, 1, 1); PG8_STAGE(PG8_SB(1, 0), b3, voffB); PG8_STAGE(PG8_SB(1, 1), b3 + hstep, voffB); PG8_STAGE_A(PG8_SA(1, 0), (last ? nA : cA), last, kb3, 0);
;             PG8_WAIT_V(8); PG8_WAIT_L(0); PG8_BAR; PG8_MMA(1, 0, At, B0); PG8_MMA(1, 1, At, B1); PG8_BAR; PG8_SCHED;
;     ...
;         }
;         if (wr == 0) PG8_BAR;
	s_add_i32 s34, s59, s33
	v_lshl_add_u64 v[218:219], v[218:219], 0, s[0:1]
	s_mov_b32 m0, s34
	ds_read_b128 v[184:187], v151 offset:49152
	ds_read_b128 v[188:191], v151 offset:50176
	ds_read_b128 v[192:195], v151 offset:51200
	ds_read_b128 v[196:199], v151 offset:52224
	ds_read_b128 v[202:205], v151 offset:53248
	ds_read_b128 v[206:209], v151 offset:54272
	ds_read_b128 v[210:213], v151 offset:55296
	ds_read_b128 v[214:217], v151 offset:56320
	global_load_lds_dwordx4 v[218:219], off
	s_add_i32 m0, s34, 0x2000
	s_add_u32 s30, s30, 0x160080
	v_lshl_add_u64 v[218:219], v[220:221], 0, s[0:1]
	s_addc_u32 s31, s31, 0
	s_add_i32 s34, s60, s33
	global_load_lds_dwordx4 v[218:219], off
	v_lshl_add_u64 v[218:219], s[30:31], 0, v[136:137]
	s_mov_b32 m0, s34
	s_nop 0
	global_load_lds_dwordx4 v[218:219], off
	v_lshl_add_u64 v[218:219], s[30:31], 0, v[140:141]
	s_add_i32 m0, s34, 0x2000
	s_nop 0
	global_load_lds_dwordx4 v[218:219], off
	v_lshl_add_u64 v[218:219], v[222:223], 0, s[0:1]
	s_mov_b32 m0, s48
	s_nop 0
	global_load_lds_dwordx4 v[218:219], off
	v_lshl_add_u64 v[218:219], v[224:225], 0, s[0:1]
	s_mov_b32 m0, s49
	s_nop 0
	global_load_lds_dwordx4 v[218:219], off
	s_waitcnt vmcnt(8)
	s_waitcnt lgkmcnt(0)
	s_barrier
	v_mfma_f32_16x16x32_bf16 v[58:61], v[152:155], v[184:187], v[58:61]
	v_mfma_f32_16x16x32_bf16 v[78:81], v[160:163], v[184:187], v[78:81]
	v_mfma_f32_16x16x32_bf16 v[66:69], v[152:155], v[192:195], v[66:69]
	v_mfma_f32_16x16x32_bf16 v[82:85], v[160:163], v[192:195], v[82:85]
	v_mfma_f32_16x16x32_bf16 v[74:77], v[152:155], v[202:205], v[74:77]
	v_mfma_f32_16x16x32_bf16 v[98:101], v[160:163], v[202:205], v[98:101]
	v_mfma_f32_16x16x32_bf16 v[90:93], v[152:155], v[210:213], v[90:93]
	v_mfma_f32_16x16x32_bf16 v[94:97], v[160:163], v[210:213], v[94:97]
	v_mfma_f32_16x16x32_bf16 v[58:61], v[156:159], v[188:191], v[58:61]
	v_mfma_f32_16x16x32_bf16 v[78:81], v[164:167], v[188:191], v[78:81]
	v_mfma_f32_16x16x32_bf16 v[66:69], v[156:159], v[196:199], v[66:69]
	v_mfma_f32_16x16x32_bf16 v[82:85], v[164:167], v[196:199], v[82:85]
	v_mfma_f32_16x16x32_bf16 v[74:77], v[156:159], v[206:209], v[74:77]
	v_mfma_f32_16x16x32_bf16 v[98:101], v[164:167], v[206:209], v[98:101]
	v_mfma_f32_16x16x32_bf16 v[90:93], v[156:159], v[214:217], v[90:93]
	v_mfma_f32_16x16x32_bf16 v[94:97], v[164:167], v[214:217], v[94:97]
	v_mfma_f32_16x16x32_bf16 v[114:117], v[168:171], v[184:187], v[114:117]
	v_mfma_f32_16x16x32_bf16 v[130:133], v[176:179], v[184:187], v[130:133]
	v_mfma_f32_16x16x32_bf16 v[110:113], v[168:171], v[192:195], v[110:113]
	v_mfma_f32_16x16x32_bf16 v[126:129], v[176:179], v[192:195], v[126:129]
	v_mfma_f32_16x16x32_bf16 v[106:109], v[168:171], v[202:205], v[106:109]
	v_mfma_f32_16x16x32_bf16 v[122:125], v[176:179], v[202:205], v[122:125]
	v_mfma_f32_16x16x32_bf16 v[102:105], v[168:171], v[210:213], v[102:105]
	v_mfma_f32_16x16x32_bf16 v[118:121], v[176:179], v[210:213], v[118:121]
	v_mfma_f32_16x16x32_bf16 v[114:117], v[172:175], v[188:191], v[114:117]
	v_mfma_f32_16x16x32_bf16 v[130:133], v[180:183], v[188:191], v[130:133]
	v_mfma_f32_16x16x32_bf16 v[110:113], v[172:175], v[196:199], v[110:113]
	v_mfma_f32_16x16x32_bf16 v[126:129], v[180:183], v[196:199], v[126:129]
	v_mfma_f32_16x16x32_bf16 v[106:109], v[172:175], v[206:209], v[106:109]
	v_mfma_f32_16x16x32_bf16 v[122:125], v[180:183], v[206:209], v[122:125]
	v_mfma_f32_16x16x32_bf16 v[102:105], v[172:175], v[214:217], v[102:105]
	v_mfma_f32_16x16x32_bf16 v[118:121], v[180:183], v[214:217], v[118:121]
	s_barrier
	s_add_i32 s58, s58, 2
	s_cmpk_gt_u32 s58, 0x55
	s_mov_b64 s[34:35], s[28:29]
	s_cbranch_scc0 .LBB0_1483
	s_and_b64 vcc, exec, s[16:17]
	s_cbranch_vccz .LBB0_1486
	s_barrier

; #define PG8_STAGE_A(bufoff, base_, nx_, kb_, h_) do { if (GATHER) { if (nx_) PG8_STAGE_G(bufoff, kb_, goN, h_); else PG8_STAGE_G(bufoff, kb_, goC, h_); } \
;         else PG8_STAGE(bufoff, (base_) + (kb_) + (h_) * hstep, voffA); } while (0)
; #define PG8_STAGE(bufoff, gbase, voff) do { _Pragma("unroll") for (int _i = 0; _i < 2; ++_i) \
;         __builtin_amdgcn_global_load_lds((const unsigned*)((const char*)(gbase) + (voff)[_i]), (LAS unsigned*)(lds + (bufoff) + ldsw + _i * 8192), 16, 0, 0); } while (0)
; #define PG8_LDA(dst, b, h) do { _Pragma("unroll") for (int m = 0; m < 4; ++m) _Pragma("unroll") for (int k = 0; k < 2; ++k) dst[m][k] = *(const LAS bf16x8*)(lds + PG8_SA(b, h) + aoff + m * 2048 + k * 1024); } while (0)
; #define PG8_LDB(dst, b, h) do { _Pragma("unroll") for (int n = 0; n < 2; ++n) _Pragma("unroll") for (int k = 0; k < 2; ++k) dst[n][k] = *(const LAS bf16x8*)(lds + PG8_SB(b, h) + boff + n * 2048 + k * 1024); } while (0)
; #define PG8_MMA(ai, bj, At, Bt) do { __builtin_amdgcn_s_setprio(1); _Pragma("unroll") for (int m = 0; m < 4; ++m) _Pragma("unroll") for (int n = 0; n < 2; ++n) _Pragma("unroll") for (int k = 0; k < 2; ++k) \
;         acc[ai][bj][m][n] = __builtin_amdgcn_mfma_f32_16x16x32_bf16(Bt[n][k], At[m][k], acc[ai][bj][m][n], 0, 0, 0); __builtin_amdgcn_s_setprio(0); } while (0)
; #define PG8_WAIT_V(n) asm volatile("s_waitcnt vmcnt(" #n ")" ::: "memory")
; #define PG8_WAIT_L(n) asm volatile("s_waitcnt lgkmcnt(" #n ")" ::: "memory")
; #define PG8_BAR __builtin_amdgcn_s_barrier()
; #define PG8_SCHED __builtin_amdgcn_sched_barrier(0)
; template <class Epi, class Sched, bool GATHER = false>
; __device__ __forceinline__ void gemm_phase(LAS unsigned char* lds, const Gemm g, const Sched& S, const Epi& E, const int tid) {
;     ...
;             PG8_LDB(B0, 0, 0); PG8_LDB(B1, 0, 1); PG8_SCHED; PG8_LDA(At, 0, 0); PG8_STAGE_A(PG8_SA(1, 1), cA, false, kb1, 1);
;             PG8_WAIT_V(8); PG8_WAIT_L(0); PG8_BAR; PG8_MMA(0, 0, At, B0); PG8_MMA(0, 1, At, B1); PG8_BAR; PG8_SCHED;
;             PG8_LDA(At, 0, 1); PG8_STAGE(PG8_SB(0, 0), b2, voffB); PG8_STAGE(PG8_SB(0, 1), b2 + hstep, voffB); PG8_STAGE_A(PG8_SA(0, 0), (last ? nA : cA), last, kb2, 0);
;             PG8_WAIT_V(8); PG8_WAIT_L(0); PG8_BAR; PG8_MMA(1, 0, At, B0); PG8_MMA(1, 1, At, B1); PG8_BAR; PG8_SCHED;
.LBB0_1505:
	s_add_u32 s30, s34, 0x100
	s_addc_u32 s31, s35, 0
	s_add_i32 s64, 0, 0x10000
	s_add_i32 s65, 0, 0x14000
	v_add_u32_e32 v2, s64, v153
	ds_read_b128 v[158:161], v2
	ds_read_b128 v[162:165], v2 offset:1024
	ds_read_b128 v[166:169], v2 offset:2048
	ds_read_b128 v[170:173], v2 offset:3072
	v_add_u32_e32 v2, s65, v153
	ds_read_b128 v[174:177], v2
	ds_read_b128 v[178:181], v2 offset:1024
	ds_read_b128 v[182:185], v2 offset:2048
	ds_read_b128 v[186:189], v2 offset:3072
	s_add_i32 s67, s64, s48
	s_add_i32 m0, s51, 0xc000
	s_add_i32 s66, s51, 0xe000
	s_add_i32 s68, s67, 0x2000
	s_cmp_eq_u32 s63, 40
	v_lshl_add_u64 v[190:191], v[4:5], 0, s[34:35]
	s_cselect_b64 vcc, -1, 0
	v_cndmask_b32_e32 v199, v191, v147, vcc
	v_cndmask_b32_e32 v198, v190, v146, vcc
	s_cselect_b32 s64, 0, s30
	v_lshl_add_u64 v[226:227], v[148:149], 0, s[34:35]
	ds_read_b128 v[190:193], v155
	ds_read_b128 v[194:197], v155 offset:1024
	ds_read_b128 v[202:205], v155 offset:2048
	ds_read_b128 v[206:209], v155 offset:3072
	ds_read_b128 v[210:213], v155 offset:4096
	ds_read_b128 v[214:217], v155 offset:5120
	ds_read_b128 v[218:221], v155 offset:6144
	ds_read_b128 v[222:225], v155 offset:7168
	global_load_lds_dwordx4 v[226:227], off
	v_lshl_add_u64 v[226:227], v[150:151], 0, s[34:35]
	s_mov_b32 m0, s66
	s_nop 0
	global_load_lds_dwordx4 v[226:227], off
	s_waitcnt vmcnt(8)
	s_waitcnt lgkmcnt(0)
	s_barrier
	v_mfma_f32_16x16x32_bf16 v[90:93], v[158:161], v[190:193], v[90:93]
	v_mfma_f32_16x16x32_bf16 v[18:21], v[166:169], v[190:193], v[18:21]
	v_mfma_f32_16x16x32_bf16 v[6:9], v[158:161], v[202:205], v[6:9]
	v_mfma_f32_16x16x32_bf16 v[22:25], v[166:169], v[202:205], v[22:25]
	v_mfma_f32_16x16x32_bf16 v[10:13], v[158:161], v[210:213], v[10:13]
	v_mfma_f32_16x16x32_bf16 v[26:29], v[166:169], v[210:213], v[26:29]
	v_mfma_f32_16x16x32_bf16 v[14:17], v[158:161], v[218:221], v[14:17]
	v_mfma_f32_16x16x32_bf16 v[30:33], v[166:169], v[218:221], v[30:33]
	v_mfma_f32_16x16x32_bf16 v[90:93], v[162:165], v[194:197], v[90:93]
	v_mfma_f32_16x16x32_bf16 v[18:21], v[170:173], v[194:197], v[18:21]
	v_mfma_f32_16x16x32_bf16 v[6:9], v[162:165], v[206:209], v[6:9]
	v_mfma_f32_16x16x32_bf16 v[22:25], v[170:173], v[206:209], v[22:25]
	v_mfma_f32_16x16x32_bf16 v[10:13], v[162:165], v[214:217], v[10:13]
	v_mfma_f32_16x16x32_bf16 v[26:29], v[170:173], v[214:217], v[26:29]
	v_mfma_f32_16x16x32_bf16 v[14:17], v[162:165], v[222:225], v[14:17]
	v_mfma_f32_16x16x32_bf16 v[30:33], v[170:173], v[222:225], v[30:33]
	v_mfma_f32_16x16x32_bf16 v[34:37], v[174:177], v[190:193], v[34:37]
	v_mfma_f32_16x16x32_bf16 v[50:53], v[182:185], v[190:193], v[50:53]
	v_mfma_f32_16x16x32_bf16 v[38:41], v[174:177], v[202:205], v[38:41]
	v_mfma_f32_16x16x32_bf16 v[54:57], v[182:185], v[202:205], v[54:57]
	v_mfma_f32_16x16x32_bf16 v[42:45], v[174:177], v[210:213], v[42:45]
	v_mfma_f32_16x16x32_bf16 v[62:65], v[182:185], v[210:213], v[62:65]
	v_mfma_f32_16x16x32_bf16 v[46:49], v[174:177], v[218:221], v[46:49]
	v_mfma_f32_16x16x32_bf16 v[70:73], v[182:185], v[218:221], v[70:73]
	v_mfma_f32_16x16x32_bf16 v[34:37], v[178:181], v[194:197], v[34:37]
	v_mfma_f32_16x16x32_bf16 v[50:53], v[186:189], v[194:197], v[50:53]
	v_mfma_f32_16x16x32_bf16 v[38:41], v[178:181], v[206:209], v[38:41]
	v_mfma_f32_16x16x32_bf16 v[54:57], v[186:189], v[206:209], v[54:57]
	v_mfma_f32_16x16x32_bf16 v[42:45], v[178:181], v[214:217], v[42:45]
	v_mfma_f32_16x16x32_bf16 v[62:65], v[186:189], v[214:217], v[62:65]
	v_mfma_f32_16x16x32_bf16 v[46:49], v[178:181], v[222:225], v[46:49]
	v_mfma_f32_16x16x32_bf16 v[70:73], v[186:189], v[222:225], v[70:73]
	s_barrier
	s_mov_b32 m0, s67
	v_lshl_add_u64 v[226:227], v[198:199], 0, v[138:139]
	ds_read_b128 v[190:193], v155 offset:16384
	ds_read_b128 v[194:197], v155 offset:17408
	ds_read_b128 v[202:205], v155 offset:18432
	ds_read_b128 v[206:209], v155 offset:19456
	ds_read_b128 v[210:213], v155 offset:20480
	ds_read_b128 v[214:217], v155 offset:21504
	ds_read_b128 v[218:221], v155 offset:22528
	ds_read_b128 v[222:225], v155 offset:23552
	global_load_lds_dwordx4 v[226:227], off
	v_lshl_add_u64 v[228:229], v[198:199], 0, v[134:135]
	s_mov_b32 m0, s68
	s_cselect_b32 s35, s11, s29
	s_cselect_b32 s34, s10, s28
	v_lshl_add_u64 v[230:231], v[198:199], 0, s[72:73]
	s_add_i32 s65, s65, s48
	global_load_lds_dwordx4 v[228:229], off
	v_lshl_add_u64 v[232:233], v[230:231], 0, v[138:139]
	s_mov_b32 m0, s65
	v_lshl_add_u64 v[230:231], v[230:231], 0, v[134:135]
	global_load_lds_dwordx4 v[232:233], off
	s_add_i32 m0, s65, 0x2000
	s_add_u32 s34, s34, s64
	s_addc_u32 s35, s35, 0
	global_load_lds_dwordx4 v[230:231], off
	v_lshl_add_u64 v[230:231], s[34:35], 0, v[140:141]
	s_mov_b32 m0, s51
	v_lshl_add_u64 v[232:233], s[34:35], 0, v[136:137]
	global_load_lds_dwordx4 v[230:231], off
	s_mov_b32 m0, s52
	s_nop 0
	global_load_lds_dwordx4 v[232:233], off
	s_waitcnt vmcnt(8)
	s_waitcnt lgkmcnt(0)
	s_barrier
; #define PG8_STAGE_A(bufoff, base_, nx_, kb_, h_) do { if (GATHER) { if (nx_) PG8_STAGE_G(bufoff, kb_, goN, h_); else PG8_STAGE_G(bufoff, kb_, goC, h_); } \
;         else PG8_STAGE(bufoff, (base_) + (kb_) + (h_) * hstep, voffA); } while (0)
; #define PG8_LDA(dst, b, h) do { _Pragma("unroll") for (int m = 0; m < 4; ++m) _Pragma("unroll") for (int k = 0; k < 2; ++k) dst[m][k] = *(const LAS bf16x8*)(lds + PG8_SA(b, h) + aoff + m * 2048 + k * 1024); } while (0)
; #define PG8_LDB(dst, b, h) do { _Pragma("unroll") for (int n = 0; n < 2; ++n) _Pragma("unroll") for (int k = 0; k < 2; ++k) dst[n][k] = *(const LAS bf16x8*)(lds + PG8_SB(b, h) + boff + n * 2048 + k * 1024); } while (0)
; #define PG8_MMA(ai, bj, At, Bt) do { __builtin_amdgcn_s_setprio(1); _Pragma("unroll") for (int m = 0; m < 4; ++m) _Pragma("unroll") for (int n = 0; n < 2; ++n) _Pragma("unroll") for (int k = 0; k < 2; ++k) \
;         acc[ai][bj][m][n] = __builtin_amdgcn_mfma_f32_16x16x32_bf16(Bt[n][k], At[m][k], acc[ai][bj][m][n], 0, 0, 0); __builtin_amdgcn_s_setprio(0); } while (0)
; #define PG8_WAIT_V(n) asm volatile("s_waitcnt vmcnt(" #n ")" ::: "memory")
; #define PG8_WAIT_L(n) asm volatile("s_waitcnt lgkmcnt(" #n ")" ::: "memory")
; #define PG8_BAR __builtin_amdgcn_s_barrier()
; #define PG8_SCHED __builtin_amdgcn_sched_barrier(0)
; template <class Epi, class Sched, bool GATHER = false>
; __device__ __forceinline__ void gemm_phase(LAS unsigned char* lds, const Gemm g, const Sched& S, const Epi& E, const int tid) {
;     ...
;             PG8_WAIT_V(8); PG8_WAIT_L(0); PG8_BAR; PG8_MMA(1, 0, At, B0); PG8_MMA(1, 1, At, B1); PG8_BAR; PG8_SCHED;
;             PG8_LDB(B0, 1, 0); PG8_LDB(B1, 1, 1); PG8_SCHED; PG8_LDA(At, 1, 0); PG8_STAGE_A(PG8_SA(0, 1), (last ? nA : cA), last, kb2, 1);
;             PG8_WAIT_V(8); PG8_WAIT_L(0); PG8_BAR; PG8_MMA(0, 0, At, B0); PG8_MMA(0, 1, At, B1); PG8_BAR; PG8_SCHED;
	v_mfma_f32_16x16x32_bf16 v[58:61], v[158:161], v[190:193], v[58:61]
	v_mfma_f32_16x16x32_bf16 v[78:81], v[166:169], v[190:193], v[78:81]
	v_mfma_f32_16x16x32_bf16 v[66:69], v[158:161], v[202:205], v[66:69]
	v_mfma_f32_16x16x32_bf16 v[82:85], v[166:169], v[202:205], v[82:85]
	v_mfma_f32_16x16x32_bf16 v[74:77], v[158:161], v[210:213], v[74:77]
	v_mfma_f32_16x16x32_bf16 v[86:89], v[166:169], v[210:213], v[86:89]
	v_mfma_f32_16x16x32_bf16 v[94:97], v[158:161], v[218:221], v[94:97]
	v_mfma_f32_16x16x32_bf16 v[98:101], v[166:169], v[218:221], v[98:101]
	v_mfma_f32_16x16x32_bf16 v[58:61], v[162:165], v[194:197], v[58:61]
	v_mfma_f32_16x16x32_bf16 v[78:81], v[170:173], v[194:197], v[78:81]
	v_mfma_f32_16x16x32_bf16 v[66:69], v[162:165], v[206:209], v[66:69]
	v_mfma_f32_16x16x32_bf16 v[82:85], v[170:173], v[206:209], v[82:85]
	v_mfma_f32_16x16x32_bf16 v[74:77], v[162:165], v[214:217], v[74:77]
	v_mfma_f32_16x16x32_bf16 v[86:89], v[170:173], v[214:217], v[86:89]
	v_mfma_f32_16x16x32_bf16 v[94:97], v[162:165], v[222:225], v[94:97]
	v_mfma_f32_16x16x32_bf16 v[98:101], v[170:173], v[222:225], v[98:101]
	v_mfma_f32_16x16x32_bf16 v[114:117], v[174:177], v[190:193], v[114:117]
	v_mfma_f32_16x16x32_bf16 v[130:133], v[182:185], v[190:193], v[130:133]
	v_mfma_f32_16x16x32_bf16 v[110:113], v[174:177], v[202:205], v[110:113]
	v_mfma_f32_16x16x32_bf16 v[126:129], v[182:185], v[202:205], v[126:129]
	v_mfma_f32_16x16x32_bf16 v[106:109], v[174:177], v[210:213], v[106:109]
	v_mfma_f32_16x16x32_bf16 v[122:125], v[182:185], v[210:213], v[122:125]
	v_mfma_f32_16x16x32_bf16 v[102:105], v[174:177], v[218:221], v[102:105]
	v_mfma_f32_16x16x32_bf16 v[118:121], v[182:185], v[218:221], v[118:121]
	v_mfma_f32_16x16x32_bf16 v[114:117], v[178:181], v[194:197], v[114:117]
	v_mfma_f32_16x16x32_bf16 v[130:133], v[186:189], v[194:197], v[130:133]
	v_mfma_f32_16x16x32_bf16 v[110:113], v[178:181], v[206:209], v[110:113]
	v_mfma_f32_16x16x32_bf16 v[126:129], v[186:189], v[206:209], v[126:129]
	v_mfma_f32_16x16x32_bf16 v[106:109], v[178:181], v[214:217], v[106:109]
	v_mfma_f32_16x16x32_bf16 v[122:125], v[186:189], v[214:217], v[122:125]
	v_mfma_f32_16x16x32_bf16 v[102:105], v[178:181], v[222:225], v[102:105]
	v_mfma_f32_16x16x32_bf16 v[118:121], v[186:189], v[222:225], v[118:121]
	s_barrier
	s_add_i32 s64, 0, 0x18000
	v_add_u32_e32 v2, s64, v153
	s_add_i32 s65, 0, 0x1c000
	ds_read_b128 v[158:161], v2
	ds_read_b128 v[162:165], v2 offset:1024
	ds_read_b128 v[166:169], v2 offset:2048
	ds_read_b128 v[170:173], v2 offset:3072
	v_add_u32_e32 v2, s65, v153
	ds_read_b128 v[174:177], v2
	ds_read_b128 v[178:181], v2 offset:1024
	ds_read_b128 v[182:185], v2 offset:2048
	ds_read_b128 v[186:189], v2 offset:3072
	s_add_u32 s34, s34, 0xb0000
	s_addc_u32 s35, s35, 0
	s_mov_b32 m0, s53
	v_lshl_add_u64 v[234:235], s[34:35], 0, v[140:141]
	ds_read_b128 v[190:193], v155 offset:32768
	ds_read_b128 v[194:197], v155 offset:33792
	ds_read_b128 v[202:205], v155 offset:34816
	ds_read_b128 v[206:209], v155 offset:35840
	ds_read_b128 v[210:213], v155 offset:36864
	ds_read_b128 v[214:217], v155 offset:37888
	ds_read_b128 v[218:221], v155 offset:38912
	ds_read_b128 v[222:225], v155 offset:39936
	global_load_lds_dwordx4 v[234:235], off
	v_lshl_add_u64 v[234:235], s[34:35], 0, v[136:137]
	s_mov_b32 m0, s54
	s_nop 0
	global_load_lds_dwordx4 v[234:235], off
	s_waitcnt vmcnt(8)
	s_waitcnt lgkmcnt(0)
	s_barrier
	v_mfma_f32_16x16x32_bf16 v[90:93], v[158:161], v[190:193], v[90:93]
	v_mfma_f32_16x16x32_bf16 v[18:21], v[166:169], v[190:193], v[18:21]
	v_mfma_f32_16x16x32_bf16 v[6:9], v[158:161], v[202:205], v[6:9]
	v_mfma_f32_16x16x32_bf16 v[22:25], v[166:169], v[202:205], v[22:25]
	v_mfma_f32_16x16x32_bf16 v[10:13], v[158:161], v[210:213], v[10:13]
	v_mfma_f32_16x16x32_bf16 v[26:29], v[166:169], v[210:213], v[26:29]
	v_mfma_f32_16x16x32_bf16 v[14:17], v[158:161], v[218:221], v[14:17]
	v_mfma_f32_16x16x32_bf16 v[30:33], v[166:169], v[218:221], v[30:33]
	v_mfma_f32_16x16x32_bf16 v[90:93], v[162:165], v[194:197], v[90:93]
	v_mfma_f32_16x16x32_bf16 v[18:21], v[170:173], v[194:197], v[18:21]
	v_mfma_f32_16x16x32_bf16 v[6:9], v[162:165], v[206:209], v[6:9]
	v_mfma_f32_16x16x32_bf16 v[22:25], v[170:173], v[206:209], v[22:25]
	v_mfma_f32_16x16x32_bf16 v[10:13], v[162:165], v[214:217], v[10:13]
	v_mfma_f32_16x16x32_bf16 v[26:29], v[170:173], v[214:217], v[26:29]
	v_mfma_f32_16x16x32_bf16 v[14:17], v[162:165], v[222:225], v[14:17]
	v_mfma_f32_16x16x32_bf16 v[30:33], v[170:173], v[222:225], v[30:33]
	v_mfma_f32_16x16x32_bf16 v[34:37], v[174:177], v[190:193], v[34:37]
	v_mfma_f32_16x16x32_bf16 v[50:53], v[182:185], v[190:193], v[50:53]
	v_mfma_f32_16x16x32_bf16 v[38:41], v[174:177], v[202:205], v[38:41]
	v_mfma_f32_16x16x32_bf16 v[54:57], v[182:185], v[202:205], v[54:57]
	v_mfma_f32_16x16x32_bf16 v[42:45], v[174:177], v[210:213], v[42:45]
	v_mfma_f32_16x16x32_bf16 v[62:65], v[182:185], v[210:213], v[62:65]
	v_mfma_f32_16x16x32_bf16 v[46:49], v[174:177], v[218:221], v[46:49]
	v_mfma_f32_16x16x32_bf16 v[70:73], v[182:185], v[218:221], v[70:73]
	v_mfma_f32_16x16x32_bf16 v[34:37], v[178:181], v[194:197], v[34:37]
	v_mfma_f32_16x16x32_bf16 v[50:53], v[186:189], v[194:197], v[50:53]
	v_mfma_f32_16x16x32_bf16 v[38:41], v[178:181], v[206:209], v[38:41]
	v_mfma_f32_16x16x32_bf16 v[54:57], v[186:189], v[206:209], v[54:57]
	v_mfma_f32_16x16x32_bf16 v[42:45], v[178:181], v[214:217], v[42:45]
	v_mfma_f32_16x16x32_bf16 v[62:65], v[186:189], v[214:217], v[62:65]
	v_mfma_f32_16x16x32_bf16 v[46:49], v[178:181], v[222:225], v[46:49]
	v_mfma_f32_16x16x32_bf16 v[70:73], v[186:189], v[222:225], v[70:73]
	s_barrier
; #define PG8_STAGE_A(bufoff, base_, nx_, kb_, h_) do { if (GATHER) { if (nx_) PG8_STAGE_G(bufoff, kb_, goN, h_); else PG8_STAGE_G(bufoff, kb_, goC, h_); } \
;         else PG8_STAGE(bufoff, (base_) + (kb_) + (h_) * hstep, voffA); } while (0)
; #define PG8_STAGE(bufoff, gbase, voff) do { _Pragma("unroll") for (int _i = 0; _i < 2; ++_i) \
;         __builtin_amdgcn_global_load_lds((const unsigned*)((const char*)(gbase) + (voff)[_i]), (LAS unsigned*)(lds + (bufoff) + ldsw + _i * 8192), 16, 0, 0); } while (0)
; #define PG8_LDA(dst, b, h) do { _Pragma("unroll") for (int m = 0; m < 4; ++m) _Pragma("unroll") for (int k = 0; k < 2; ++k) dst[m][k] = *(const LAS bf16x8*)(lds + PG8_SA(b, h) + aoff + m * 2048 + k * 1024); } while (0)
; #define PG8_MMA(ai, bj, At, Bt) do { __builtin_amdgcn_s_setprio(1); _Pragma("unroll") for (int m = 0; m < 4; ++m) _Pragma("unroll") for (int n = 0; n < 2; ++n) _Pragma("unroll") for (int k = 0; k < 2; ++k) \
;         acc[ai][bj][m][n] = __builtin_amdgcn_mfma_f32_16x16x32_bf16(Bt[n][k], At[m][k], acc[ai][bj][m][n], 0, 0, 0); __builtin_amdgcn_s_setprio(0); } while (0)
; #define PG8_WAIT_V(n) asm volatile("s_waitcnt vmcnt(" #n ")" ::: "memory")
; #define PG8_WAIT_L(n) asm volatile("s_waitcnt lgkmcnt(" #n ")" ::: "memory")
; #define PG8_BAR __builtin_amdgcn_s_barrier()
; #define PG8_SCHED __builtin_amdgcn_sched_barrier(0)
; template <class Epi, class Sched, bool GATHER = false>
; __device__ __forceinline__ void gemm_phase(LAS unsigned char* lds, const Gemm g, const Sched& S, const Epi& E, const int tid) {
;     ...
;             PG8_LDA(At, 1, 1); PG8_STAGE(PG8_SB(1, 0), b3, voffB); PG8_STAGE(PG8_SB(1, 1), b3 + hstep, voffB); PG8_STAGE_A(PG8_SA(1, 0), (last ? nA : cA), last, kb3, 0);
;             PG8_WAIT_V(8); PG8_WAIT_L(0); PG8_BAR; PG8_MMA(1, 0, At, B0); PG8_MMA(1, 1, At, B1); PG8_BAR; PG8_SCHED;
;     ...
;         }
;         if (wr == 0) PG8_BAR;
	s_add_i32 s34, s64, s48
	v_lshl_add_u64 v[226:227], v[226:227], 0, s[0:1]
	s_mov_b32 m0, s34
	ds_read_b128 v[190:193], v155 offset:49152
	ds_read_b128 v[194:197], v155 offset:50176
	ds_read_b128 v[202:205], v155 offset:51200
	ds_read_b128 v[206:209], v155 offset:52224
	ds_read_b128 v[210:213], v155 offset:53248
	ds_read_b128 v[214:217], v155 offset:54272
	ds_read_b128 v[218:221], v155 offset:55296
	ds_read_b128 v[222:225], v155 offset:56320
	global_load_lds_dwordx4 v[226:227], off
	v_lshl_add_u64 v[226:227], v[228:229], 0, s[0:1]
	s_add_i32 m0, s34, 0x2000
	v_lshl_add_u64 v[198:199], v[198:199], 0, s[76:77]
	s_add_i32 s34, s65, s48
	global_load_lds_dwordx4 v[226:227], off
	v_lshl_add_u64 v[226:227], v[198:199], 0, v[138:139]
	s_mov_b32 m0, s34
	v_lshl_add_u64 v[198:199], v[198:199], 0, v[134:135]
	global_load_lds_dwordx4 v[226:227], off
	s_add_i32 m0, s34, 0x2000
	s_nop 0
	global_load_lds_dwordx4 v[198:199], off
	v_lshl_add_u64 v[198:199], v[230:231], 0, s[0:1]
	s_mov_b32 m0, s55
	s_nop 0
	global_load_lds_dwordx4 v[198:199], off
	v_lshl_add_u64 v[198:199], v[232:233], 0, s[0:1]
	s_mov_b32 m0, s56
	s_nop 0
	global_load_lds_dwordx4 v[198:199], off
	s_waitcnt vmcnt(8)
	s_waitcnt lgkmcnt(0)
	s_barrier
	v_mfma_f32_16x16x32_bf16 v[58:61], v[158:161], v[190:193], v[58:61]
	v_mfma_f32_16x16x32_bf16 v[78:81], v[166:169], v[190:193], v[78:81]
	v_mfma_f32_16x16x32_bf16 v[66:69], v[158:161], v[202:205], v[66:69]
	v_mfma_f32_16x16x32_bf16 v[82:85], v[166:169], v[202:205], v[82:85]
	v_mfma_f32_16x16x32_bf16 v[74:77], v[158:161], v[210:213], v[74:77]
	v_mfma_f32_16x16x32_bf16 v[86:89], v[166:169], v[210:213], v[86:89]
	v_mfma_f32_16x16x32_bf16 v[94:97], v[158:161], v[218:221], v[94:97]
	v_mfma_f32_16x16x32_bf16 v[98:101], v[166:169], v[218:221], v[98:101]
	v_mfma_f32_16x16x32_bf16 v[58:61], v[162:165], v[194:197], v[58:61]
	v_mfma_f32_16x16x32_bf16 v[78:81], v[170:173], v[194:197], v[78:81]
	v_mfma_f32_16x16x32_bf16 v[66:69], v[162:165], v[206:209], v[66:69]
	v_mfma_f32_16x16x32_bf16 v[82:85], v[170:173], v[206:209], v[82:85]
	v_mfma_f32_16x16x32_bf16 v[74:77], v[162:165], v[214:217], v[74:77]
	v_mfma_f32_16x16x32_bf16 v[86:89], v[170:173], v[214:217], v[86:89]
	v_mfma_f32_16x16x32_bf16 v[94:97], v[162:165], v[222:225], v[94:97]
	v_mfma_f32_16x16x32_bf16 v[98:101], v[170:173], v[222:225], v[98:101]
	v_mfma_f32_16x16x32_bf16 v[114:117], v[174:177], v[190:193], v[114:117]
	v_mfma_f32_16x16x32_bf16 v[130:133], v[182:185], v[190:193], v[130:133]
	v_mfma_f32_16x16x32_bf16 v[110:113], v[174:177], v[202:205], v[110:113]
	v_mfma_f32_16x16x32_bf16 v[126:129], v[182:185], v[202:205], v[126:129]
	v_mfma_f32_16x16x32_bf16 v[106:109], v[174:177], v[210:213], v[106:109]
	v_mfma_f32_16x16x32_bf16 v[122:125], v[182:185], v[210:213], v[122:125]
	v_mfma_f32_16x16x32_bf16 v[102:105], v[174:177], v[218:221], v[102:105]
	v_mfma_f32_16x16x32_bf16 v[118:121], v[182:185], v[218:221], v[118:121]
	v_mfma_f32_16x16x32_bf16 v[114:117], v[178:181], v[194:197], v[114:117]
	v_mfma_f32_16x16x32_bf16 v[130:133], v[186:189], v[194:197], v[130:133]
	v_mfma_f32_16x16x32_bf16 v[110:113], v[178:181], v[206:209], v[110:113]
	v_mfma_f32_16x16x32_bf16 v[126:129], v[186:189], v[206:209], v[126:129]
	v_mfma_f32_16x16x32_bf16 v[106:109], v[178:181], v[214:217], v[106:109]
	v_mfma_f32_16x16x32_bf16 v[122:125], v[186:189], v[214:217], v[122:125]
	v_mfma_f32_16x16x32_bf16 v[102:105], v[178:181], v[222:225], v[102:105]
	v_mfma_f32_16x16x32_bf16 v[118:121], v[186:189], v[222:225], v[118:121]
	s_barrier
	s_add_i32 s63, s63, 2
	s_cmp_gt_u32 s63, 41
	s_mov_b64 s[34:35], s[30:31]
	s_cbranch_scc0 .LBB0_1505
	s_and_b64 vcc, exec, s[24:25]
	s_cbranch_vccz .LBB0_1508
	s_barrier
